# hot loop heads aligned to 32 bytes
# baseline (speedup 1.0000x reference)
.LBB0_125:
	s_mov_b32 s9, -2
	s_mov_b64 s[4:5], 0
	s_waitcnt vmcnt(8)
	.p2align 5
	s_nop 0
	ds_read_b128 v[130:133], v219
	ds_read_b128 v[134:137], v219 offset:2048
	ds_read_b128 v[138:141], v220
	ds_read_b128 v[142:145], v220 offset:2048
	ds_read_b128 v[146:149], v221
	ds_read_b128 v[150:153], v221 offset:2048
	ds_read_b128 v[154:157], v222
	ds_read_b128 v[158:161], v222 offset:2048
	ds_read_b128 v[162:165], v223
	ds_read_b128 v[166:169], v223 offset:2048
	ds_read_b128 v[170:173], v224
	ds_read_b128 v[174:177], v224 offset:2048
	ds_read_b128 v[178:181], v223 offset:4096
	ds_read_b128 v[182:185], v223 offset:6144
	ds_read_b128 v[186:189], v224 offset:4096
	ds_read_b128 v[190:193], v224 offset:6144
	s_add_u32 s47, s14, s4
	s_addc_u32 s50, s15, s5
	s_add_u32 s54, s47, 0x80
	s_addc_u32 s55, s50, 0
	s_mov_b32 m0, s70
	s_nop 0
	global_load_lds_dwordx4 v212, s[54:55] offset:0
	s_nop 0
	s_mov_b32 m0, s71
	s_nop 0
	global_load_lds_dwordx4 v214, s[54:55] offset:0
	s_waitcnt vmcnt(8)
	s_waitcnt lgkmcnt(0)
	s_barrier
	s_setprio 1
	s_waitcnt lgkmcnt(7)
	v_mfma_f32_16x16x32_bf16 v[126:129], v[130:133], v[162:165], 0
	v_mfma_f32_16x16x32_bf16 v[122:125], v[134:137], v[162:165], 0
	s_waitcnt lgkmcnt(6)
	v_mfma_f32_16x16x32_bf16 v[118:121], v[130:133], v[166:169], 0
	v_mfma_f32_16x16x32_bf16 v[114:117], v[134:137], v[166:169], 0
	s_waitcnt lgkmcnt(3)
	v_mfma_f32_16x16x32_bf16 v[110:113], v[130:133], v[178:181], 0
	v_mfma_f32_16x16x32_bf16 v[106:109], v[134:137], v[178:181], 0
	s_waitcnt lgkmcnt(2)
	v_mfma_f32_16x16x32_bf16 v[102:105], v[130:133], v[182:185], 0
	v_mfma_f32_16x16x32_bf16 v[98:101], v[134:137], v[182:185], 0
	v_mfma_f32_16x16x32_bf16 v[126:129], v[138:141], v[170:173], v[126:129]
	v_mfma_f32_16x16x32_bf16 v[122:125], v[142:145], v[170:173], v[122:125]
	v_mfma_f32_16x16x32_bf16 v[118:121], v[138:141], v[174:177], v[118:121]
	v_mfma_f32_16x16x32_bf16 v[114:117], v[142:145], v[174:177], v[114:117]
	s_waitcnt lgkmcnt(1)
	v_mfma_f32_16x16x32_bf16 v[110:113], v[138:141], v[186:189], v[110:113]
	v_mfma_f32_16x16x32_bf16 v[106:109], v[142:145], v[186:189], v[106:109]
	s_waitcnt lgkmcnt(0)
	v_mfma_f32_16x16x32_bf16 v[102:105], v[138:141], v[190:193], v[102:105]
	v_mfma_f32_16x16x32_bf16 v[98:101], v[142:145], v[190:193], v[98:101]
	s_setprio 0
	s_setprio 1
	v_mfma_f32_16x16x32_bf16 v[94:97], v[146:149], v[162:165], 0
	v_mfma_f32_16x16x32_bf16 v[90:93], v[150:153], v[162:165], 0
	v_mfma_f32_16x16x32_bf16 v[86:89], v[146:149], v[166:169], 0
	v_mfma_f32_16x16x32_bf16 v[82:85], v[150:153], v[166:169], 0
	v_mfma_f32_16x16x32_bf16 v[78:81], v[146:149], v[178:181], 0
	v_mfma_f32_16x16x32_bf16 v[74:77], v[150:153], v[178:181], 0
	v_mfma_f32_16x16x32_bf16 v[70:73], v[146:149], v[182:185], 0
	v_mfma_f32_16x16x32_bf16 v[66:69], v[150:153], v[182:185], 0
	v_mfma_f32_16x16x32_bf16 v[94:97], v[154:157], v[170:173], v[94:97]
	v_mfma_f32_16x16x32_bf16 v[90:93], v[158:161], v[170:173], v[90:93]
	v_mfma_f32_16x16x32_bf16 v[86:89], v[154:157], v[174:177], v[86:89]
	v_mfma_f32_16x16x32_bf16 v[82:85], v[158:161], v[174:177], v[82:85]
	v_mfma_f32_16x16x32_bf16 v[78:81], v[154:157], v[186:189], v[78:81]
	v_mfma_f32_16x16x32_bf16 v[74:77], v[158:161], v[186:189], v[74:77]
	v_mfma_f32_16x16x32_bf16 v[70:73], v[154:157], v[190:193], v[70:73]
	v_mfma_f32_16x16x32_bf16 v[66:69], v[158:161], v[190:193], v[66:69]
	s_setprio 0
	s_barrier
	s_add_u32 s51, s10, s4
	s_addc_u32 s53, s11, s5
	ds_read_b128 v[162:165], v223 offset:16384
	ds_read_b128 v[166:169], v223 offset:18432
	ds_read_b128 v[170:173], v224 offset:16384
	ds_read_b128 v[174:177], v224 offset:18432
	ds_read_b128 v[178:181], v223 offset:20480
	ds_read_b128 v[182:185], v223 offset:22528
	ds_read_b128 v[186:189], v224 offset:20480
	ds_read_b128 v[190:193], v224 offset:22528
	s_add_u32 s54, s51, 0x100
	s_addc_u32 s55, s53, 0
	s_mov_b32 m0, s57
	s_nop 0
	global_load_lds_dwordx4 v215, s[54:55] offset:0
	s_nop 0
	s_mov_b32 m0, s58
	s_nop 0
	global_load_lds_dwordx4 v216, s[54:55] offset:0
	s_add_u32 s54, s51, 0x40100
	s_addc_u32 s55, s53, 0
	s_mov_b32 m0, s59
	s_nop 0
	global_load_lds_dwordx4 v215, s[54:55] offset:0
	s_nop 0
	s_mov_b32 m0, s60
	s_nop 0
	global_load_lds_dwordx4 v216, s[54:55] offset:0
	s_add_u32 s54, s47, 0x100
	s_addc_u32 s55, s50, 0
	s_mov_b32 m0, s56
	s_nop 0
	global_load_lds_dwordx4 v211, s[54:55] offset:0
	s_nop 0
	s_mov_b32 m0, s61
	s_nop 0
	global_load_lds_dwordx4 v213, s[54:55] offset:0
	s_cmp_lg_u32 s9, 0xfffffffe
	s_cbranch_scc1 .Lrope_skip_ft
	s_lshl_b32 s100, s8, 14
	s_add_u32 s100, s96, s100
	s_addc_u32 s101, s97, 0
	s_mov_b32 m0, s98
	s_nop 0
	global_load_lds_dwordx4 v210, s[100:101] offset:0
	s_add_u32 s100, s100, 0x2000
	s_addc_u32 s101, s101, 0
	s_add_u32 s99, s98, 0x2000
	s_mov_b32 m0, s99
	s_nop 0
	global_load_lds_dwordx4 v210, s[100:101] offset:0

.LBB0_126:
	.p2align 5
	s_nop 0
	ds_read_b128 v[130:133], v219
	ds_read_b128 v[134:137], v219 offset:2048
	ds_read_b128 v[138:141], v220
	ds_read_b128 v[142:145], v220 offset:2048
	ds_read_b128 v[146:149], v221
	ds_read_b128 v[150:153], v221 offset:2048
	ds_read_b128 v[154:157], v222
	ds_read_b128 v[158:161], v222 offset:2048
	ds_read_b128 v[162:165], v223
	ds_read_b128 v[166:169], v223 offset:2048
	ds_read_b128 v[170:173], v224
	ds_read_b128 v[174:177], v224 offset:2048
	ds_read_b128 v[178:181], v223 offset:4096
	ds_read_b128 v[182:185], v223 offset:6144
	ds_read_b128 v[186:189], v224 offset:4096
	ds_read_b128 v[190:193], v224 offset:6144
	s_add_u32 s47, s14, s4
	s_addc_u32 s50, s15, s5
	s_add_u32 s54, s47, 0x80
	s_addc_u32 s55, s50, 0
	s_mov_b32 m0, s70
	s_nop 0
	global_load_lds_dwordx4 v212, s[54:55] offset:0
	s_nop 0
	s_mov_b32 m0, s71
	s_nop 0
	global_load_lds_dwordx4 v214, s[54:55] offset:0
	s_waitcnt vmcnt(8)
	s_waitcnt lgkmcnt(0)
	s_barrier
	s_setprio 1
	s_waitcnt lgkmcnt(7)
	v_mfma_f32_16x16x32_bf16 v[126:129], v[130:133], v[162:165], v[126:129]
	v_mfma_f32_16x16x32_bf16 v[122:125], v[134:137], v[162:165], v[122:125]
	s_waitcnt lgkmcnt(6)
	v_mfma_f32_16x16x32_bf16 v[118:121], v[130:133], v[166:169], v[118:121]
	v_mfma_f32_16x16x32_bf16 v[114:117], v[134:137], v[166:169], v[114:117]
	s_waitcnt lgkmcnt(3)
	v_mfma_f32_16x16x32_bf16 v[110:113], v[130:133], v[178:181], v[110:113]
	v_mfma_f32_16x16x32_bf16 v[106:109], v[134:137], v[178:181], v[106:109]
	s_waitcnt lgkmcnt(2)
	v_mfma_f32_16x16x32_bf16 v[102:105], v[130:133], v[182:185], v[102:105]
	v_mfma_f32_16x16x32_bf16 v[98:101], v[134:137], v[182:185], v[98:101]
	v_mfma_f32_16x16x32_bf16 v[126:129], v[138:141], v[170:173], v[126:129]
	v_mfma_f32_16x16x32_bf16 v[122:125], v[142:145], v[170:173], v[122:125]
	v_mfma_f32_16x16x32_bf16 v[118:121], v[138:141], v[174:177], v[118:121]
	v_mfma_f32_16x16x32_bf16 v[114:117], v[142:145], v[174:177], v[114:117]
	s_waitcnt lgkmcnt(1)
	v_mfma_f32_16x16x32_bf16 v[110:113], v[138:141], v[186:189], v[110:113]
	v_mfma_f32_16x16x32_bf16 v[106:109], v[142:145], v[186:189], v[106:109]
	s_waitcnt lgkmcnt(0)
	v_mfma_f32_16x16x32_bf16 v[102:105], v[138:141], v[190:193], v[102:105]
	v_mfma_f32_16x16x32_bf16 v[98:101], v[142:145], v[190:193], v[98:101]
	s_setprio 0
	s_setprio 1
	v_mfma_f32_16x16x32_bf16 v[94:97], v[146:149], v[162:165], v[94:97]
	v_mfma_f32_16x16x32_bf16 v[90:93], v[150:153], v[162:165], v[90:93]
	v_mfma_f32_16x16x32_bf16 v[86:89], v[146:149], v[166:169], v[86:89]
	v_mfma_f32_16x16x32_bf16 v[82:85], v[150:153], v[166:169], v[82:85]
	v_mfma_f32_16x16x32_bf16 v[78:81], v[146:149], v[178:181], v[78:81]
	v_mfma_f32_16x16x32_bf16 v[74:77], v[150:153], v[178:181], v[74:77]
	v_mfma_f32_16x16x32_bf16 v[70:73], v[146:149], v[182:185], v[70:73]
	v_mfma_f32_16x16x32_bf16 v[66:69], v[150:153], v[182:185], v[66:69]
	v_mfma_f32_16x16x32_bf16 v[94:97], v[154:157], v[170:173], v[94:97]
	v_mfma_f32_16x16x32_bf16 v[90:93], v[158:161], v[170:173], v[90:93]
	v_mfma_f32_16x16x32_bf16 v[86:89], v[154:157], v[174:177], v[86:89]
	v_mfma_f32_16x16x32_bf16 v[82:85], v[158:161], v[174:177], v[82:85]
	v_mfma_f32_16x16x32_bf16 v[78:81], v[154:157], v[186:189], v[78:81]
	v_mfma_f32_16x16x32_bf16 v[74:77], v[158:161], v[186:189], v[74:77]
	v_mfma_f32_16x16x32_bf16 v[70:73], v[154:157], v[190:193], v[70:73]
	v_mfma_f32_16x16x32_bf16 v[66:69], v[158:161], v[190:193], v[66:69]
	s_setprio 0
	s_barrier
	s_add_u32 s51, s10, s4
	s_addc_u32 s53, s11, s5
	ds_read_b128 v[162:165], v223 offset:16384
	ds_read_b128 v[166:169], v223 offset:18432
	ds_read_b128 v[170:173], v224 offset:16384
	ds_read_b128 v[174:177], v224 offset:18432
	ds_read_b128 v[178:181], v223 offset:20480
	ds_read_b128 v[182:185], v223 offset:22528
	ds_read_b128 v[186:189], v224 offset:20480
	ds_read_b128 v[190:193], v224 offset:22528
	s_add_u32 s54, s51, 0x100
	s_addc_u32 s55, s53, 0
	s_mov_b32 m0, s57
	s_nop 0
	global_load_lds_dwordx4 v215, s[54:55] offset:0
	s_nop 0
	s_mov_b32 m0, s58
	s_nop 0
	global_load_lds_dwordx4 v216, s[54:55] offset:0
	s_add_u32 s54, s51, 0x40100
	s_addc_u32 s55, s53, 0
	s_mov_b32 m0, s59
	s_nop 0
	global_load_lds_dwordx4 v215, s[54:55] offset:0
	s_nop 0
	s_mov_b32 m0, s60
	s_nop 0
	global_load_lds_dwordx4 v216, s[54:55] offset:0
	s_add_u32 s54, s47, 0x100
	s_addc_u32 s55, s50, 0
	s_mov_b32 m0, s56
	s_nop 0
	global_load_lds_dwordx4 v211, s[54:55] offset:0
	s_nop 0
	s_mov_b32 m0, s61
	s_nop 0
	global_load_lds_dwordx4 v213, s[54:55] offset:0
	s_cmp_lg_u32 s9, 0xfffffffe
	s_cbranch_scc1 .Lrope_skip
	s_lshl_b32 s100, s8, 14
	s_add_u32 s100, s96, s100
	s_addc_u32 s101, s97, 0
	s_mov_b32 m0, s98
	s_nop 0
	global_load_lds_dwordx4 v210, s[100:101] offset:0
	s_add_u32 s100, s100, 0x2000
	s_addc_u32 s101, s101, 0
	s_add_u32 s99, s98, 0x2000
	s_mov_b32 m0, s99
	s_nop 0
	global_load_lds_dwordx4 v210, s[100:101] offset:0

.LBB0_251:
	.p2align 5
	s_nop 0
	s_add_u32 s72, s90, s70
	s_addc_u32 s73, s91, s71
	s_add_u32 s6, s72, 0x100000
	s_addc_u32 s7, s73, 0
	s_add_u32 s88, s92, s70
	s_addc_u32 s89, s93, s71
	s_mov_b32 m0, s85
	s_nop 0
	global_load_lds_dwordx4 v168, s[6:7] offset:0
	s_add_u32 s6, s88, 0x100000
	s_addc_u32 s7, s89, 0
	s_mov_b32 m0, s86
	s_nop 0
	global_load_lds_dwordx4 v169, s[6:7] offset:0
	s_nop 0
	s_mov_b32 m0, s87
	s_nop 0
	global_load_lds_dwordx4 v170, s[6:7] offset:0
	ds_read_b128 v[66:69], v175
	ds_read_b128 v[82:85], v175 offset:4096
	ds_read_b128 v[114:117], v176
	ds_read_b128 v[184:187], v176 offset:4096
	ds_read_b128 v[196:199], v177
	ds_read_b128 v[200:203], v177 offset:4096
	ds_read_b128 v[204:207], v178
	ds_read_b128 v[208:211], v178 offset:4096
	s_waitcnt lgkmcnt(7)
	v_mfma_f32_32x32x16_bf16 v[66:81], v[66:69], v[110:113], 0
	v_exp_f32_e32 v120, v154
	v_exp_f32_e32 v121, v155
	v_exp_f32_e32 v152, v152
	v_exp_f32_e32 v153, v153
	v_exp_f32_e32 v150, v150
	v_exp_f32_e32 v151, v151
	v_exp_f32_e32 v148, v148
	s_waitcnt lgkmcnt(6)
	v_mfma_f32_32x32x16_bf16 v[82:97], v[82:85], v[110:113], 0
	v_exp_f32_e32 v149, v149
	v_exp_f32_e32 v146, v146
	v_exp_f32_e32 v147, v147
	v_exp_f32_e32 v144, v144
	v_exp_f32_e32 v145, v145
	v_exp_f32_e32 v154, v140
	v_exp_f32_e32 v155, v141
	s_waitcnt lgkmcnt(5)
	v_mfma_f32_32x32x16_bf16 v[66:81], v[114:117], v[106:109], v[66:81]
	v_exp_f32_e32 v116, v142
	v_exp_f32_e32 v117, v143
	v_pk_add_f32 v[114:115], v[126:127], v[144:145]
	v_pk_add_f32 v[140:141], v[134:135], v[152:153]
	v_pk_add_f32 v[142:143], v[122:123], v[154:155]
	v_pk_add_f32 v[212:213], v[136:137], v[120:121]
	v_pk_add_f32 v[214:215], v[124:125], v[116:117]
	s_waitcnt lgkmcnt(4)
	v_mfma_f32_32x32x16_bf16 v[82:97], v[184:187], v[106:109], v[82:97]
	v_pk_add_f32 v[184:185], v[130:131], v[148:149]
	v_pk_add_f32 v[186:187], v[128:129], v[146:147]
	v_pk_add_f32 v[216:217], v[132:133], v[150:151]
	v_pk_add_f32 v[186:187], v[212:213], v[186:187]
	v_pk_add_f32 v[214:215], v[216:217], v[214:215]
	v_pk_add_f32 v[142:143], v[184:185], v[142:143]
	v_pk_add_f32 v[114:115], v[140:141], v[114:115]
	s_waitcnt lgkmcnt(3)
	v_mfma_f32_32x32x16_bf16 v[66:81], v[196:199], v[102:105], v[66:81]
	v_pk_add_f32 v[114:115], v[114:115], v[142:143]
	v_pk_add_f32 v[140:141], v[186:187], v[214:215]
	v_pk_add_f32 v[114:115], v[140:141], v[114:115]
	v_cvt_pk_bf16_f32 v140, v136, v137
	v_cvt_pk_bf16_f32 v141, v134, v135
	v_cvt_pk_bf16_f32 v142, v132, v133
	s_waitcnt lgkmcnt(2)
	v_mfma_f32_32x32x16_bf16 v[82:97], v[200:203], v[102:105], v[82:97]
	v_pk_add_f32 v[114:115], v[114:115], v[114:115] op_sel:[0,1] op_sel_hi:[1,0]
	v_cvt_pk_bf16_f32 v143, v130, v131
	v_cvt_pk_bf16_f32 v128, v128, v129
	v_cvt_pk_bf16_f32 v129, v126, v127
	v_cvt_pk_bf16_f32 v130, v124, v125
	v_cvt_pk_bf16_f32 v131, v122, v123
	s_nop 0
	v_mov_b32_e32 v115, v114
	s_waitcnt lgkmcnt(1)
	v_mfma_f32_32x32x16_bf16 v[66:81], v[204:207], v[98:101], v[66:81]
	v_permlane32_swap_b32_e32 v114, v115
	v_cvt_pk_bf16_f32 v120, v120, v121
	v_cvt_pk_bf16_f32 v121, v152, v153
	v_cvt_pk_bf16_f32 v122, v150, v151
	v_cvt_pk_bf16_f32 v123, v148, v149
	v_cvt_pk_bf16_f32 v124, v146, v147
	s_waitcnt lgkmcnt(0)
	v_mfma_f32_32x32x16_bf16 v[82:97], v[208:211], v[98:101], v[82:97]
	v_cvt_pk_bf16_f32 v125, v144, v145
	v_cvt_pk_bf16_f32 v126, v116, v117
	v_cvt_pk_bf16_f32 v127, v154, v155
	v_permlane32_swap_b32_e32 v140, v142
	v_permlane32_swap_b32_e32 v141, v143
	v_permlane32_swap_b32_e32 v128, v130
	v_permlane32_swap_b32_e32 v129, v131
	v_permlane32_swap_b32_e32 v120, v122
	v_permlane32_swap_b32_e32 v121, v123
	v_permlane32_swap_b32_e32 v124, v126
	v_permlane32_swap_b32_e32 v125, v127
	ds_read_b64_tr_b16 v[132:133], v166 offset:0x8000
	ds_read_b64_tr_b16 v[134:135], v166 offset:0x8800
	ds_read_b64_tr_b16 v[144:145], v166 offset:0x9000
	ds_read_b64_tr_b16 v[146:147], v166 offset:0x9800
	ds_read_b64_tr_b16 v[148:149], v166 offset:0xa000
	ds_read_b64_tr_b16 v[150:151], v166 offset:0xa800
	ds_read_b64_tr_b16 v[152:153], v166 offset:0xb000
	ds_read_b64_tr_b16 v[154:155], v166 offset:0xb800
	ds_read_b64_tr_b16 v[184:185], v166 offset:0x8200
	ds_read_b64_tr_b16 v[186:187], v166 offset:0x8a00
	ds_read_b64_tr_b16 v[196:197], v166 offset:0x9200
	ds_read_b64_tr_b16 v[198:199], v166 offset:0x9a00
	ds_read_b64_tr_b16 v[200:201], v166 offset:0xa200
	ds_read_b64_tr_b16 v[202:203], v166 offset:0xaa00
	ds_read_b64_tr_b16 v[204:205], v166 offset:0xb200
	ds_read_b64_tr_b16 v[206:207], v166 offset:0xba00
	s_waitcnt lgkmcnt(8)
	s_nop 0
	v_mfma_f32_32x32x16_bf16 v[18:33], v[140:143], v[132:135], v[18:33]
	v_mfma_f32_32x32x16_bf16 v[18:33], v[128:131], v[144:147], v[18:33]
	v_mfma_f32_32x32x16_bf16 v[18:33], v[120:123], v[148:151], v[18:33]
	v_mfma_f32_32x32x16_bf16 v[18:33], v[124:127], v[152:155], v[18:33]
	ds_read_b64_tr_b16 v[132:133], v166 offset:0x8400
	ds_read_b64_tr_b16 v[134:135], v166 offset:0x8c00
	ds_read_b64_tr_b16 v[144:145], v166 offset:0x9400
	ds_read_b64_tr_b16 v[146:147], v166 offset:0x9c00
	ds_read_b64_tr_b16 v[148:149], v166 offset:0xa400
	ds_read_b64_tr_b16 v[150:151], v166 offset:0xac00
	ds_read_b64_tr_b16 v[152:153], v166 offset:0xb400
	ds_read_b64_tr_b16 v[154:155], v166 offset:0xbc00
	s_waitcnt lgkmcnt(8)
	v_mfma_f32_32x32x16_bf16 v[34:49], v[140:143], v[184:187], v[34:49]
	v_mfma_f32_32x32x16_bf16 v[34:49], v[128:131], v[196:199], v[34:49]
	v_mfma_f32_32x32x16_bf16 v[34:49], v[120:123], v[200:203], v[34:49]
	v_mfma_f32_32x32x16_bf16 v[34:49], v[124:127], v[204:207], v[34:49]
	ds_read_b64_tr_b16 v[184:185], v166 offset:0x8600
	ds_read_b64_tr_b16 v[186:187], v166 offset:0x8e00
	ds_read_b64_tr_b16 v[196:197], v166 offset:0x9600
	ds_read_b64_tr_b16 v[198:199], v166 offset:0x9e00
	ds_read_b64_tr_b16 v[200:201], v166 offset:0xa600
	ds_read_b64_tr_b16 v[202:203], v166 offset:0xae00
	ds_read_b64_tr_b16 v[204:205], v166 offset:0xb600
	ds_read_b64_tr_b16 v[206:207], v166 offset:0xbe00
	s_waitcnt lgkmcnt(8)
	v_mfma_f32_32x32x16_bf16 v[50:65], v[140:143], v[132:135], v[50:65]
	v_mfma_f32_32x32x16_bf16 v[50:65], v[128:131], v[144:147], v[50:65]
	v_mfma_f32_32x32x16_bf16 v[50:65], v[120:123], v[148:151], v[50:65]
	v_mfma_f32_32x32x16_bf16 v[50:65], v[124:127], v[152:155], v[50:65]
	s_waitcnt lgkmcnt(0)
	v_mfma_f32_32x32x16_bf16 v[2:17], v[140:143], v[184:187], v[2:17]
	s_add_i32 s6, s95, 0xffffff40
	s_cmp_le_i32 s6, s77
	v_mfma_f32_32x32x16_bf16 v[2:17], v[128:131], v[196:199], v[2:17]
	v_mfma_f32_32x32x16_bf16 v[2:17], v[120:123], v[200:203], v[2:17]
	v_mfma_f32_32x32x16_bf16 v[2:17], v[124:127], v[204:207], v[2:17]
	s_cbranch_scc1 .LBB0_253
	v_cmp_gt_i32_e64 s[66:67], 26, v183
	v_cmp_gt_i32_e64 s[68:69], 27, v183
	v_cmp_gt_i32_e64 s[64:65], 25, v183
	s_and_b64 s[66:67], s[68:69], s[66:67]
	v_cmp_gt_i32_e64 s[62:63], 24, v183
	s_and_b64 s[64:65], s[66:67], s[64:65]
	v_cmp_gt_i32_e64 s[60:61], 19, v183
	s_and_b64 s[62:63], s[64:65], s[62:63]
	v_cmp_gt_i32_e64 s[58:59], 18, v183
	s_and_b64 s[60:61], s[62:63], s[60:61]
	v_cmp_gt_i32_e64 s[56:57], 17, v183
	s_and_b64 s[58:59], s[60:61], s[58:59]
	v_cmp_gt_i32_e64 s[54:55], 16, v183
	s_and_b64 s[56:57], s[58:59], s[56:57]
	v_cmp_gt_i32_e64 s[52:53], 11, v183
	s_and_b64 s[54:55], s[56:57], s[54:55]
	v_cmp_gt_i32_e64 s[50:51], 10, v183
	s_and_b64 s[52:53], s[54:55], s[52:53]
	v_cmp_gt_i32_e64 s[48:49], 9, v183
	s_and_b64 s[50:51], s[52:53], s[50:51]
	v_cmp_gt_i32_e64 s[44:45], 8, v183
	s_and_b64 s[48:49], s[50:51], s[48:49]
	v_cmp_gt_i32_e64 s[42:43], 3, v183
	s_and_b64 s[44:45], s[48:49], s[44:45]
	v_cmp_gt_i32_e64 s[40:41], 2, v183
	s_and_b64 s[42:43], s[44:45], s[42:43]
	v_cmp_gt_i32_e64 s[38:39], 1, v183
	s_and_b64 s[40:41], s[42:43], s[40:41]
	v_cmp_gt_i32_e64 s[36:37], 0, v183
	s_and_b64 s[38:39], s[40:41], s[38:39]
	s_and_b64 s[36:37], s[38:39], s[36:37]
	v_cmp_gt_i32_e64 s[34:35], 58, v183
	v_cndmask_b32_e64 v66, v66, v160, s[36:37]
	v_cmp_gt_i32_e64 s[36:37], 59, v183
	v_cmp_gt_i32_e64 s[30:31], 57, v183
	s_and_b64 s[34:35], s[36:37], s[34:35]
	v_cmp_gt_i32_e64 s[28:29], 56, v183
	s_and_b64 s[30:31], s[34:35], s[30:31]
	v_cmp_gt_i32_e64 s[26:27], 51, v183
	s_and_b64 s[28:29], s[30:31], s[28:29]
	v_cmp_gt_i32_e64 s[24:25], 50, v183
	s_and_b64 s[26:27], s[28:29], s[26:27]
	v_cmp_gt_i32_e64 s[22:23], 49, v183
	s_and_b64 s[24:25], s[26:27], s[24:25]
	v_cmp_gt_i32_e64 s[20:21], 48, v183
	s_and_b64 s[22:23], s[24:25], s[22:23]
	v_cmp_gt_i32_e64 s[18:19], 43, v183
	s_and_b64 s[20:21], s[22:23], s[20:21]
	v_cmp_gt_i32_e64 s[16:17], 42, v183
	s_and_b64 s[18:19], s[20:21], s[18:19]
	v_cmp_gt_i32_e64 s[14:15], 41, v183
	s_and_b64 s[16:17], s[18:19], s[16:17]
	v_cmp_gt_i32_e64 s[12:13], 40, v183
	s_and_b64 s[14:15], s[16:17], s[14:15]
	v_cmp_gt_i32_e64 s[10:11], 35, v183
	s_and_b64 s[12:13], s[14:15], s[12:13]
	v_cmp_gt_i32_e64 s[8:9], 34, v183
	s_and_b64 s[10:11], s[12:13], s[10:11]
	v_cmp_gt_i32_e64 s[6:7], 33, v183
	s_and_b64 s[8:9], s[10:11], s[8:9]
	v_cmp_gt_i32_e32 vcc, 32, v183
	s_and_b64 s[6:7], s[8:9], s[6:7]
	s_and_b64 vcc, s[6:7], vcc
	v_cndmask_b32_e64 v81, v81, v160, s[68:69]
	v_cndmask_b32_e64 v80, v80, v160, s[66:67]
	v_cndmask_b32_e64 v79, v79, v160, s[64:65]
	v_cndmask_b32_e64 v78, v78, v160, s[62:63]
	v_cndmask_b32_e64 v77, v77, v160, s[60:61]
	v_cndmask_b32_e64 v76, v76, v160, s[58:59]
	v_cndmask_b32_e64 v75, v75, v160, s[56:57]
	v_cndmask_b32_e64 v74, v74, v160, s[54:55]
	v_cndmask_b32_e64 v73, v73, v160, s[52:53]
	v_cndmask_b32_e64 v72, v72, v160, s[50:51]
	v_cndmask_b32_e64 v71, v71, v160, s[48:49]
	v_cndmask_b32_e64 v70, v70, v160, s[44:45]
	v_cndmask_b32_e64 v69, v69, v160, s[42:43]
	v_cndmask_b32_e64 v68, v68, v160, s[40:41]
	v_cndmask_b32_e64 v67, v67, v160, s[38:39]
	v_cndmask_b32_e64 v97, v97, v160, s[36:37]
	v_cndmask_b32_e64 v96, v96, v160, s[34:35]
	v_cndmask_b32_e64 v95, v95, v160, s[30:31]
	v_cndmask_b32_e64 v94, v94, v160, s[28:29]
	v_cndmask_b32_e64 v93, v93, v160, s[26:27]
	v_cndmask_b32_e64 v92, v92, v160, s[24:25]
	v_cndmask_b32_e64 v91, v91, v160, s[22:23]
	v_cndmask_b32_e64 v90, v90, v160, s[20:21]
	v_cndmask_b32_e64 v89, v89, v160, s[18:19]
	v_cndmask_b32_e64 v88, v88, v160, s[16:17]
	v_cndmask_b32_e64 v87, v87, v160, s[14:15]
	v_cndmask_b32_e64 v86, v86, v160, s[12:13]
	v_cndmask_b32_e64 v85, v85, v160, s[10:11]
	v_cndmask_b32_e64 v84, v84, v160, s[8:9]
	v_cndmask_b32_e64 v83, v83, v160, s[6:7]
	v_cndmask_b32_e32 v82, v82, v160, vcc

.LBB0_367:
	s_mov_b32 s31, -2
	s_mov_b64 s[6:7], 0
	.p2align 5
	s_nop 0
	ds_read_b128 v[130:133], v203
	ds_read_b128 v[134:137], v203 offset:2048
	ds_read_b128 v[138:141], v204
	ds_read_b128 v[142:145], v204 offset:2048
	ds_read_b128 v[146:149], v205
	ds_read_b128 v[150:153], v205 offset:2048
	ds_read_b128 v[154:157], v206
	ds_read_b128 v[158:161], v206 offset:2048
	ds_read_b128 v[162:165], v207
	ds_read_b128 v[166:169], v207 offset:2048
	ds_read_b128 v[174:177], v208
	ds_read_b128 v[178:181], v208 offset:2048
	ds_read_b128 v[182:185], v207 offset:4096
	ds_read_b128 v[210:213], v207 offset:6144
	ds_read_b128 v[214:217], v208 offset:4096
	ds_read_b128 v[218:221], v208 offset:6144
	s_add_u32 s36, s8, s6
	s_addc_u32 s37, s9, s7
	s_add_u32 s58, s36, 0x80
	s_addc_u32 s59, s37, 0
	s_mov_b32 m0, s52
	s_nop 0
	global_load_lds_dwordx4 v198, s[58:59] offset:0
	s_nop 0
	s_mov_b32 m0, s53
	s_nop 0
	global_load_lds_dwordx4 v200, s[58:59] offset:0
	s_waitcnt vmcnt(8)
	s_waitcnt lgkmcnt(0)
	s_barrier
	s_setprio 1
	s_waitcnt lgkmcnt(7)
	v_mfma_f32_16x16x32_bf16 v[126:129], v[130:133], v[162:165], 0
	v_mfma_f32_16x16x32_bf16 v[122:125], v[134:137], v[162:165], 0
	s_waitcnt lgkmcnt(6)
	v_mfma_f32_16x16x32_bf16 v[118:121], v[130:133], v[166:169], 0
	v_mfma_f32_16x16x32_bf16 v[114:117], v[134:137], v[166:169], 0
	s_waitcnt lgkmcnt(3)
	v_mfma_f32_16x16x32_bf16 v[110:113], v[130:133], v[182:185], 0
	v_mfma_f32_16x16x32_bf16 v[106:109], v[134:137], v[182:185], 0
	s_waitcnt lgkmcnt(2)
	v_mfma_f32_16x16x32_bf16 v[102:105], v[130:133], v[210:213], 0
	v_mfma_f32_16x16x32_bf16 v[98:101], v[134:137], v[210:213], 0
	v_mfma_f32_16x16x32_bf16 v[126:129], v[138:141], v[174:177], v[126:129]
	v_mfma_f32_16x16x32_bf16 v[122:125], v[142:145], v[174:177], v[122:125]
	v_mfma_f32_16x16x32_bf16 v[118:121], v[138:141], v[178:181], v[118:121]
	v_mfma_f32_16x16x32_bf16 v[114:117], v[142:145], v[178:181], v[114:117]
	s_waitcnt lgkmcnt(1)
	v_mfma_f32_16x16x32_bf16 v[110:113], v[138:141], v[214:217], v[110:113]
	v_mfma_f32_16x16x32_bf16 v[106:109], v[142:145], v[214:217], v[106:109]
	s_waitcnt lgkmcnt(0)
	v_mfma_f32_16x16x32_bf16 v[102:105], v[138:141], v[218:221], v[102:105]
	v_mfma_f32_16x16x32_bf16 v[98:101], v[142:145], v[218:221], v[98:101]
	s_setprio 0
	s_setprio 1
	v_mfma_f32_16x16x32_bf16 v[94:97], v[146:149], v[162:165], 0
	v_mfma_f32_16x16x32_bf16 v[90:93], v[150:153], v[162:165], 0
	v_mfma_f32_16x16x32_bf16 v[86:89], v[146:149], v[166:169], 0
	v_mfma_f32_16x16x32_bf16 v[82:85], v[150:153], v[166:169], 0
	v_mfma_f32_16x16x32_bf16 v[78:81], v[146:149], v[182:185], 0
	v_mfma_f32_16x16x32_bf16 v[74:77], v[150:153], v[182:185], 0
	v_mfma_f32_16x16x32_bf16 v[70:73], v[146:149], v[210:213], 0
	v_mfma_f32_16x16x32_bf16 v[66:69], v[150:153], v[210:213], 0
	v_mfma_f32_16x16x32_bf16 v[94:97], v[154:157], v[174:177], v[94:97]
	v_mfma_f32_16x16x32_bf16 v[90:93], v[158:161], v[174:177], v[90:93]
	v_mfma_f32_16x16x32_bf16 v[86:89], v[154:157], v[178:181], v[86:89]
	v_mfma_f32_16x16x32_bf16 v[82:85], v[158:161], v[178:181], v[82:85]
	v_mfma_f32_16x16x32_bf16 v[78:81], v[154:157], v[214:217], v[78:81]
	v_mfma_f32_16x16x32_bf16 v[74:77], v[158:161], v[214:217], v[74:77]
	v_mfma_f32_16x16x32_bf16 v[70:73], v[154:157], v[218:221], v[70:73]
	v_mfma_f32_16x16x32_bf16 v[66:69], v[158:161], v[218:221], v[66:69]
	s_setprio 0
	s_barrier
	s_add_u32 s60, s34, s6
	s_addc_u32 s61, s35, s7
	ds_read_b128 v[162:165], v207 offset:16384
	ds_read_b128 v[166:169], v207 offset:18432
	ds_read_b128 v[174:177], v208 offset:16384
	ds_read_b128 v[178:181], v208 offset:18432
	ds_read_b128 v[182:185], v207 offset:20480
	ds_read_b128 v[210:213], v207 offset:22528
	ds_read_b128 v[214:217], v208 offset:20480
	ds_read_b128 v[218:221], v208 offset:22528
	s_add_u32 s58, s60, 0x100
	s_addc_u32 s59, s61, 0
	s_mov_b32 m0, s39
	s_nop 0
	global_load_lds_dwordx4 v195, s[58:59] offset:0
	s_nop 0
	s_mov_b32 m0, s40
	s_nop 0
	global_load_lds_dwordx4 v196, s[58:59] offset:0
	s_add_u32 s58, s60, 0x40100
	s_addc_u32 s59, s61, 0
	s_mov_b32 m0, s41
	s_nop 0
	global_load_lds_dwordx4 v195, s[58:59] offset:0
	s_nop 0
	s_mov_b32 m0, s42
	s_nop 0
	global_load_lds_dwordx4 v196, s[58:59] offset:0
	s_add_u32 s58, s36, 0x100
	s_addc_u32 s59, s37, 0
	s_mov_b32 m0, s38
	s_nop 0
	global_load_lds_dwordx4 v197, s[58:59] offset:0
	s_nop 0
	s_mov_b32 m0, s43
	s_nop 0
	global_load_lds_dwordx4 v199, s[58:59] offset:0
	s_waitcnt vmcnt(8)
	s_waitcnt lgkmcnt(0)
	s_barrier
	s_setprio 1
	s_waitcnt lgkmcnt(7)
	v_mfma_f32_16x16x32_bf16 v[62:65], v[130:133], v[162:165], 0
	v_mfma_f32_16x16x32_bf16 v[58:61], v[134:137], v[162:165], 0
	s_waitcnt lgkmcnt(6)
	v_mfma_f32_16x16x32_bf16 v[54:57], v[130:133], v[166:169], 0
	v_mfma_f32_16x16x32_bf16 v[50:53], v[134:137], v[166:169], 0
	s_waitcnt lgkmcnt(3)
	v_mfma_f32_16x16x32_bf16 v[46:49], v[130:133], v[182:185], 0
	v_mfma_f32_16x16x32_bf16 v[42:45], v[134:137], v[182:185], 0
	s_waitcnt lgkmcnt(2)
	v_mfma_f32_16x16x32_bf16 v[38:41], v[130:133], v[210:213], 0
	v_mfma_f32_16x16x32_bf16 v[34:37], v[134:137], v[210:213], 0
	v_mfma_f32_16x16x32_bf16 v[62:65], v[138:141], v[174:177], v[62:65]
	v_mfma_f32_16x16x32_bf16 v[58:61], v[142:145], v[174:177], v[58:61]
	v_mfma_f32_16x16x32_bf16 v[54:57], v[138:141], v[178:181], v[54:57]
	v_mfma_f32_16x16x32_bf16 v[50:53], v[142:145], v[178:181], v[50:53]
	s_waitcnt lgkmcnt(1)
	v_mfma_f32_16x16x32_bf16 v[46:49], v[138:141], v[214:217], v[46:49]
	v_mfma_f32_16x16x32_bf16 v[42:45], v[142:145], v[214:217], v[42:45]
	s_waitcnt lgkmcnt(0)
	v_mfma_f32_16x16x32_bf16 v[38:41], v[138:141], v[218:221], v[38:41]
	v_mfma_f32_16x16x32_bf16 v[34:37], v[142:145], v[218:221], v[34:37]
	s_setprio 0
	s_setprio 1
	v_mfma_f32_16x16x32_bf16 v[30:33], v[146:149], v[162:165], 0
	v_mfma_f32_16x16x32_bf16 v[26:29], v[150:153], v[162:165], 0
	v_mfma_f32_16x16x32_bf16 v[22:25], v[146:149], v[166:169], 0
	v_mfma_f32_16x16x32_bf16 v[18:21], v[150:153], v[166:169], 0
	v_mfma_f32_16x16x32_bf16 v[14:17], v[146:149], v[182:185], 0
	v_mfma_f32_16x16x32_bf16 v[10:13], v[150:153], v[182:185], 0
	v_mfma_f32_16x16x32_bf16 v[6:9], v[146:149], v[210:213], 0
	v_mfma_f32_16x16x32_bf16 v[2:5], v[150:153], v[210:213], 0
	v_mfma_f32_16x16x32_bf16 v[30:33], v[154:157], v[174:177], v[30:33]
	v_mfma_f32_16x16x32_bf16 v[26:29], v[158:161], v[174:177], v[26:29]
	v_mfma_f32_16x16x32_bf16 v[22:25], v[154:157], v[178:181], v[22:25]
	v_mfma_f32_16x16x32_bf16 v[18:21], v[158:161], v[178:181], v[18:21]
	v_mfma_f32_16x16x32_bf16 v[14:17], v[154:157], v[214:217], v[14:17]
	v_mfma_f32_16x16x32_bf16 v[10:13], v[158:161], v[214:217], v[10:13]
	v_mfma_f32_16x16x32_bf16 v[6:9], v[154:157], v[218:221], v[6:9]
	v_mfma_f32_16x16x32_bf16 v[2:5], v[158:161], v[218:221], v[2:5]
	s_setprio 0
	s_barrier
	s_add_i32 s62, 0, 0x18000
	v_add_u32_e32 v174, s62, v201
	v_add_u32_e32 v175, s62, v202
	s_add_i32 s62, 0, 0x1c000
	v_add_u32_e32 v176, s62, v201
	ds_read_b128 v[130:133], v174
	ds_read_b128 v[134:137], v174 offset:2048
	ds_read_b128 v[138:141], v175
	ds_read_b128 v[142:145], v175 offset:2048
	v_add_u32_e32 v177, s62, v202
	ds_read_b128 v[146:149], v176
	ds_read_b128 v[150:153], v176 offset:2048
	ds_read_b128 v[154:157], v177
	ds_read_b128 v[158:161], v177 offset:2048
	ds_read_b128 v[162:165], v207 offset:32768
	ds_read_b128 v[166:169], v207 offset:34816
	ds_read_b128 v[178:181], v208 offset:32768
	ds_read_b128 v[182:185], v208 offset:34816
	ds_read_b128 v[210:213], v207 offset:36864
	ds_read_b128 v[214:217], v207 offset:38912
	ds_read_b128 v[218:221], v208 offset:36864
	ds_read_b128 v[222:225], v208 offset:38912
	s_mov_b32 m0, s44
	s_nop 0
	global_load_lds_dwordx4 v198, s[58:59] offset:0
	s_nop 0
	s_mov_b32 m0, s45
	s_nop 0
	global_load_lds_dwordx4 v200, s[58:59] offset:0
	s_waitcnt vmcnt(8)
	s_waitcnt lgkmcnt(0)
	s_barrier
	s_setprio 1
	s_waitcnt lgkmcnt(7)
	v_mfma_f32_16x16x32_bf16 v[126:129], v[130:133], v[162:165], v[126:129]
	v_mfma_f32_16x16x32_bf16 v[122:125], v[134:137], v[162:165], v[122:125]
	s_waitcnt lgkmcnt(6)
	v_mfma_f32_16x16x32_bf16 v[118:121], v[130:133], v[166:169], v[118:121]
	v_mfma_f32_16x16x32_bf16 v[114:117], v[134:137], v[166:169], v[114:117]
	s_waitcnt lgkmcnt(3)
	v_mfma_f32_16x16x32_bf16 v[110:113], v[130:133], v[210:213], v[110:113]
	v_mfma_f32_16x16x32_bf16 v[106:109], v[134:137], v[210:213], v[106:109]
	s_waitcnt lgkmcnt(2)
	v_mfma_f32_16x16x32_bf16 v[102:105], v[130:133], v[214:217], v[102:105]
	v_mfma_f32_16x16x32_bf16 v[98:101], v[134:137], v[214:217], v[98:101]
	v_mfma_f32_16x16x32_bf16 v[126:129], v[138:141], v[178:181], v[126:129]
	v_mfma_f32_16x16x32_bf16 v[122:125], v[142:145], v[178:181], v[122:125]
	v_mfma_f32_16x16x32_bf16 v[118:121], v[138:141], v[182:185], v[118:121]
	v_mfma_f32_16x16x32_bf16 v[114:117], v[142:145], v[182:185], v[114:117]
	s_waitcnt lgkmcnt(1)
	v_mfma_f32_16x16x32_bf16 v[110:113], v[138:141], v[218:221], v[110:113]
	v_mfma_f32_16x16x32_bf16 v[106:109], v[142:145], v[218:221], v[106:109]
	s_waitcnt lgkmcnt(0)
	v_mfma_f32_16x16x32_bf16 v[102:105], v[138:141], v[222:225], v[102:105]
	v_mfma_f32_16x16x32_bf16 v[98:101], v[142:145], v[222:225], v[98:101]
	s_setprio 0
	s_setprio 1
	v_mfma_f32_16x16x32_bf16 v[94:97], v[146:149], v[162:165], v[94:97]
	v_mfma_f32_16x16x32_bf16 v[90:93], v[150:153], v[162:165], v[90:93]
	v_mfma_f32_16x16x32_bf16 v[86:89], v[146:149], v[166:169], v[86:89]
	v_mfma_f32_16x16x32_bf16 v[82:85], v[150:153], v[166:169], v[82:85]
	v_mfma_f32_16x16x32_bf16 v[78:81], v[146:149], v[210:213], v[78:81]
	v_mfma_f32_16x16x32_bf16 v[74:77], v[150:153], v[210:213], v[74:77]
	v_mfma_f32_16x16x32_bf16 v[70:73], v[146:149], v[214:217], v[70:73]
	v_mfma_f32_16x16x32_bf16 v[66:69], v[150:153], v[214:217], v[66:69]
	v_mfma_f32_16x16x32_bf16 v[94:97], v[154:157], v[178:181], v[94:97]
	v_mfma_f32_16x16x32_bf16 v[90:93], v[158:161], v[178:181], v[90:93]
	v_mfma_f32_16x16x32_bf16 v[86:89], v[154:157], v[182:185], v[86:89]
	v_mfma_f32_16x16x32_bf16 v[82:85], v[158:161], v[182:185], v[82:85]
	v_mfma_f32_16x16x32_bf16 v[78:81], v[154:157], v[218:221], v[78:81]
	v_mfma_f32_16x16x32_bf16 v[74:77], v[158:161], v[218:221], v[74:77]
	v_mfma_f32_16x16x32_bf16 v[70:73], v[154:157], v[222:225], v[70:73]
	v_mfma_f32_16x16x32_bf16 v[66:69], v[158:161], v[222:225], v[66:69]
	s_setprio 0
	s_barrier
	ds_read_b128 v[162:165], v207 offset:49152
	ds_read_b128 v[166:169], v207 offset:51200
	ds_read_b128 v[178:181], v208 offset:49152
	ds_read_b128 v[182:185], v208 offset:51200
	ds_read_b128 v[210:213], v207 offset:53248
	ds_read_b128 v[214:217], v207 offset:55296
	ds_read_b128 v[218:221], v208 offset:53248
	ds_read_b128 v[222:225], v208 offset:55296
	s_add_u32 s58, s60, 0x180
	s_addc_u32 s59, s61, 0
	s_mov_b32 m0, s46
	s_nop 0
	global_load_lds_dwordx4 v195, s[58:59] offset:0
	s_nop 0
	s_mov_b32 m0, s47
	s_nop 0
	global_load_lds_dwordx4 v196, s[58:59] offset:0
	s_add_u32 s58, s60, 0x40180
	s_addc_u32 s59, s61, 0
	s_mov_b32 m0, s50
	s_nop 0
	global_load_lds_dwordx4 v195, s[58:59] offset:0
	s_add_u32 s36, s36, 0x180
	s_mov_b32 m0, s51
	s_nop 0
	global_load_lds_dwordx4 v196, s[58:59] offset:0
	s_addc_u32 s37, s37, 0
	s_mov_b32 m0, s48
	s_nop 0
	global_load_lds_dwordx4 v197, s[36:37] offset:0
	s_nop 0
	s_mov_b32 m0, s49
	s_nop 0
	global_load_lds_dwordx4 v199, s[36:37] offset:0
	s_waitcnt vmcnt(8)
	s_waitcnt lgkmcnt(0)
	s_barrier
	s_setprio 1
	s_waitcnt lgkmcnt(7)
	v_mfma_f32_16x16x32_bf16 v[62:65], v[130:133], v[162:165], v[62:65]
	v_mfma_f32_16x16x32_bf16 v[58:61], v[134:137], v[162:165], v[58:61]
	s_waitcnt lgkmcnt(6)
	v_mfma_f32_16x16x32_bf16 v[54:57], v[130:133], v[166:169], v[54:57]
	v_mfma_f32_16x16x32_bf16 v[50:53], v[134:137], v[166:169], v[50:53]
	s_waitcnt lgkmcnt(3)
	v_mfma_f32_16x16x32_bf16 v[46:49], v[130:133], v[210:213], v[46:49]
	v_mfma_f32_16x16x32_bf16 v[42:45], v[134:137], v[210:213], v[42:45]
	s_waitcnt lgkmcnt(2)
	v_mfma_f32_16x16x32_bf16 v[38:41], v[130:133], v[214:217], v[38:41]
	v_mfma_f32_16x16x32_bf16 v[34:37], v[134:137], v[214:217], v[34:37]
	v_mfma_f32_16x16x32_bf16 v[62:65], v[138:141], v[178:181], v[62:65]
	v_mfma_f32_16x16x32_bf16 v[58:61], v[142:145], v[178:181], v[58:61]
	v_mfma_f32_16x16x32_bf16 v[54:57], v[138:141], v[182:185], v[54:57]
	v_mfma_f32_16x16x32_bf16 v[50:53], v[142:145], v[182:185], v[50:53]
	s_waitcnt lgkmcnt(1)
	v_mfma_f32_16x16x32_bf16 v[46:49], v[138:141], v[218:221], v[46:49]
	v_mfma_f32_16x16x32_bf16 v[42:45], v[142:145], v[218:221], v[42:45]
	s_waitcnt lgkmcnt(0)
	v_mfma_f32_16x16x32_bf16 v[38:41], v[138:141], v[222:225], v[38:41]
	v_mfma_f32_16x16x32_bf16 v[34:37], v[142:145], v[222:225], v[34:37]
	s_setprio 0
	s_setprio 1
	v_mfma_f32_16x16x32_bf16 v[30:33], v[146:149], v[162:165], v[30:33]
	v_mfma_f32_16x16x32_bf16 v[26:29], v[150:153], v[162:165], v[26:29]
	v_mfma_f32_16x16x32_bf16 v[22:25], v[146:149], v[166:169], v[22:25]
	v_mfma_f32_16x16x32_bf16 v[18:21], v[150:153], v[166:169], v[18:21]
	v_mfma_f32_16x16x32_bf16 v[14:17], v[146:149], v[210:213], v[14:17]
	v_mfma_f32_16x16x32_bf16 v[10:13], v[150:153], v[210:213], v[10:13]
	v_mfma_f32_16x16x32_bf16 v[6:9], v[146:149], v[214:217], v[6:9]
	v_mfma_f32_16x16x32_bf16 v[2:5], v[150:153], v[214:217], v[2:5]
	v_mfma_f32_16x16x32_bf16 v[30:33], v[154:157], v[178:181], v[30:33]
	v_mfma_f32_16x16x32_bf16 v[26:29], v[158:161], v[178:181], v[26:29]
	v_mfma_f32_16x16x32_bf16 v[22:25], v[154:157], v[182:185], v[22:25]
	v_mfma_f32_16x16x32_bf16 v[18:21], v[158:161], v[182:185], v[18:21]
	v_mfma_f32_16x16x32_bf16 v[14:17], v[154:157], v[218:221], v[14:17]
	v_mfma_f32_16x16x32_bf16 v[10:13], v[158:161], v[218:221], v[10:13]
	v_mfma_f32_16x16x32_bf16 v[6:9], v[154:157], v[222:225], v[6:9]
	v_mfma_f32_16x16x32_bf16 v[2:5], v[158:161], v[222:225], v[2:5]
	s_setprio 0
	s_add_i32 s31, s31, 2
	s_add_u32 s6, s6, 0x100
	s_addc_u32 s7, s7, 0
	s_barrier
.LBB0_368:
	.p2align 5
	s_nop 0
	ds_read_b128 v[130:133], v203
	ds_read_b128 v[134:137], v203 offset:2048
	ds_read_b128 v[138:141], v204
	ds_read_b128 v[142:145], v204 offset:2048
	ds_read_b128 v[146:149], v205
	ds_read_b128 v[150:153], v205 offset:2048
	ds_read_b128 v[154:157], v206
	ds_read_b128 v[158:161], v206 offset:2048
	ds_read_b128 v[162:165], v207
	ds_read_b128 v[166:169], v207 offset:2048
	ds_read_b128 v[174:177], v208
	ds_read_b128 v[178:181], v208 offset:2048
	ds_read_b128 v[182:185], v207 offset:4096
	ds_read_b128 v[210:213], v207 offset:6144
	ds_read_b128 v[214:217], v208 offset:4096
	ds_read_b128 v[218:221], v208 offset:6144
	s_add_u32 s36, s8, s6
	s_addc_u32 s37, s9, s7
	s_add_u32 s58, s36, 0x80
	s_addc_u32 s59, s37, 0
	s_mov_b32 m0, s52
	s_nop 0
	global_load_lds_dwordx4 v198, s[58:59] offset:0
	s_nop 0
	s_mov_b32 m0, s53
	s_nop 0
	global_load_lds_dwordx4 v200, s[58:59] offset:0
	s_waitcnt vmcnt(8)
	s_waitcnt lgkmcnt(0)
	s_barrier
	s_setprio 1
	s_waitcnt lgkmcnt(7)
	v_mfma_f32_16x16x32_bf16 v[126:129], v[130:133], v[162:165], v[126:129]
	v_mfma_f32_16x16x32_bf16 v[122:125], v[134:137], v[162:165], v[122:125]
	s_waitcnt lgkmcnt(6)
	v_mfma_f32_16x16x32_bf16 v[118:121], v[130:133], v[166:169], v[118:121]
	v_mfma_f32_16x16x32_bf16 v[114:117], v[134:137], v[166:169], v[114:117]
	s_waitcnt lgkmcnt(3)
	v_mfma_f32_16x16x32_bf16 v[110:113], v[130:133], v[182:185], v[110:113]
	v_mfma_f32_16x16x32_bf16 v[106:109], v[134:137], v[182:185], v[106:109]
	s_waitcnt lgkmcnt(2)
	v_mfma_f32_16x16x32_bf16 v[102:105], v[130:133], v[210:213], v[102:105]
	v_mfma_f32_16x16x32_bf16 v[98:101], v[134:137], v[210:213], v[98:101]
	v_mfma_f32_16x16x32_bf16 v[126:129], v[138:141], v[174:177], v[126:129]
	v_mfma_f32_16x16x32_bf16 v[122:125], v[142:145], v[174:177], v[122:125]
	v_mfma_f32_16x16x32_bf16 v[118:121], v[138:141], v[178:181], v[118:121]
	v_mfma_f32_16x16x32_bf16 v[114:117], v[142:145], v[178:181], v[114:117]
	s_waitcnt lgkmcnt(1)
	v_mfma_f32_16x16x32_bf16 v[110:113], v[138:141], v[214:217], v[110:113]
	v_mfma_f32_16x16x32_bf16 v[106:109], v[142:145], v[214:217], v[106:109]
	s_waitcnt lgkmcnt(0)
	v_mfma_f32_16x16x32_bf16 v[102:105], v[138:141], v[218:221], v[102:105]
	v_mfma_f32_16x16x32_bf16 v[98:101], v[142:145], v[218:221], v[98:101]
	s_setprio 0
	s_setprio 1
	v_mfma_f32_16x16x32_bf16 v[94:97], v[146:149], v[162:165], v[94:97]
	v_mfma_f32_16x16x32_bf16 v[90:93], v[150:153], v[162:165], v[90:93]
	v_mfma_f32_16x16x32_bf16 v[86:89], v[146:149], v[166:169], v[86:89]
	v_mfma_f32_16x16x32_bf16 v[82:85], v[150:153], v[166:169], v[82:85]
	v_mfma_f32_16x16x32_bf16 v[78:81], v[146:149], v[182:185], v[78:81]
	v_mfma_f32_16x16x32_bf16 v[74:77], v[150:153], v[182:185], v[74:77]
	v_mfma_f32_16x16x32_bf16 v[70:73], v[146:149], v[210:213], v[70:73]
	v_mfma_f32_16x16x32_bf16 v[66:69], v[150:153], v[210:213], v[66:69]
	v_mfma_f32_16x16x32_bf16 v[94:97], v[154:157], v[174:177], v[94:97]
	v_mfma_f32_16x16x32_bf16 v[90:93], v[158:161], v[174:177], v[90:93]
	v_mfma_f32_16x16x32_bf16 v[86:89], v[154:157], v[178:181], v[86:89]
	v_mfma_f32_16x16x32_bf16 v[82:85], v[158:161], v[178:181], v[82:85]
	v_mfma_f32_16x16x32_bf16 v[78:81], v[154:157], v[214:217], v[78:81]
	v_mfma_f32_16x16x32_bf16 v[74:77], v[158:161], v[214:217], v[74:77]
	v_mfma_f32_16x16x32_bf16 v[70:73], v[154:157], v[218:221], v[70:73]
	v_mfma_f32_16x16x32_bf16 v[66:69], v[158:161], v[218:221], v[66:69]
	s_setprio 0
	s_barrier
	s_add_u32 s60, s34, s6
	s_addc_u32 s61, s35, s7
	ds_read_b128 v[162:165], v207 offset:16384
	ds_read_b128 v[166:169], v207 offset:18432
	ds_read_b128 v[174:177], v208 offset:16384
	ds_read_b128 v[178:181], v208 offset:18432
	ds_read_b128 v[182:185], v207 offset:20480
	ds_read_b128 v[210:213], v207 offset:22528
	ds_read_b128 v[214:217], v208 offset:20480
	ds_read_b128 v[218:221], v208 offset:22528
	s_add_u32 s58, s60, 0x100
	s_addc_u32 s59, s61, 0
	s_mov_b32 m0, s39
	s_nop 0
	global_load_lds_dwordx4 v195, s[58:59] offset:0
	s_nop 0
	s_mov_b32 m0, s40
	s_nop 0
	global_load_lds_dwordx4 v196, s[58:59] offset:0
	s_add_u32 s58, s60, 0x40100
	s_addc_u32 s59, s61, 0
	s_mov_b32 m0, s41
	s_nop 0
	global_load_lds_dwordx4 v195, s[58:59] offset:0
	s_nop 0
	s_mov_b32 m0, s42
	s_nop 0
	global_load_lds_dwordx4 v196, s[58:59] offset:0
	s_add_u32 s58, s36, 0x100
	s_addc_u32 s59, s37, 0
	s_mov_b32 m0, s38
	s_nop 0
	global_load_lds_dwordx4 v197, s[58:59] offset:0
	s_nop 0
	s_mov_b32 m0, s43
	s_nop 0
	global_load_lds_dwordx4 v199, s[58:59] offset:0
	s_waitcnt vmcnt(8)
	s_waitcnt lgkmcnt(0)
	s_barrier
	s_setprio 1
	s_waitcnt lgkmcnt(7)
	v_mfma_f32_16x16x32_bf16 v[62:65], v[130:133], v[162:165], v[62:65]
	v_mfma_f32_16x16x32_bf16 v[58:61], v[134:137], v[162:165], v[58:61]
	s_waitcnt lgkmcnt(6)
	v_mfma_f32_16x16x32_bf16 v[54:57], v[130:133], v[166:169], v[54:57]
	v_mfma_f32_16x16x32_bf16 v[50:53], v[134:137], v[166:169], v[50:53]
	s_waitcnt lgkmcnt(3)
	v_mfma_f32_16x16x32_bf16 v[46:49], v[130:133], v[182:185], v[46:49]
	v_mfma_f32_16x16x32_bf16 v[42:45], v[134:137], v[182:185], v[42:45]
	s_waitcnt lgkmcnt(2)
	v_mfma_f32_16x16x32_bf16 v[38:41], v[130:133], v[210:213], v[38:41]
	v_mfma_f32_16x16x32_bf16 v[34:37], v[134:137], v[210:213], v[34:37]
	v_mfma_f32_16x16x32_bf16 v[62:65], v[138:141], v[174:177], v[62:65]
	v_mfma_f32_16x16x32_bf16 v[58:61], v[142:145], v[174:177], v[58:61]
	v_mfma_f32_16x16x32_bf16 v[54:57], v[138:141], v[178:181], v[54:57]
	v_mfma_f32_16x16x32_bf16 v[50:53], v[142:145], v[178:181], v[50:53]
	s_waitcnt lgkmcnt(1)
	v_mfma_f32_16x16x32_bf16 v[46:49], v[138:141], v[214:217], v[46:49]
	v_mfma_f32_16x16x32_bf16 v[42:45], v[142:145], v[214:217], v[42:45]
	s_waitcnt lgkmcnt(0)
	v_mfma_f32_16x16x32_bf16 v[38:41], v[138:141], v[218:221], v[38:41]
	v_mfma_f32_16x16x32_bf16 v[34:37], v[142:145], v[218:221], v[34:37]
	s_setprio 0
	s_setprio 1
	v_mfma_f32_16x16x32_bf16 v[30:33], v[146:149], v[162:165], v[30:33]
	v_mfma_f32_16x16x32_bf16 v[26:29], v[150:153], v[162:165], v[26:29]
	v_mfma_f32_16x16x32_bf16 v[22:25], v[146:149], v[166:169], v[22:25]
	v_mfma_f32_16x16x32_bf16 v[18:21], v[150:153], v[166:169], v[18:21]
	v_mfma_f32_16x16x32_bf16 v[14:17], v[146:149], v[182:185], v[14:17]
	v_mfma_f32_16x16x32_bf16 v[10:13], v[150:153], v[182:185], v[10:13]
	v_mfma_f32_16x16x32_bf16 v[6:9], v[146:149], v[210:213], v[6:9]
	v_mfma_f32_16x16x32_bf16 v[2:5], v[150:153], v[210:213], v[2:5]
	v_mfma_f32_16x16x32_bf16 v[30:33], v[154:157], v[174:177], v[30:33]
	v_mfma_f32_16x16x32_bf16 v[26:29], v[158:161], v[174:177], v[26:29]
	v_mfma_f32_16x16x32_bf16 v[22:25], v[154:157], v[178:181], v[22:25]
	v_mfma_f32_16x16x32_bf16 v[18:21], v[158:161], v[178:181], v[18:21]
	v_mfma_f32_16x16x32_bf16 v[14:17], v[154:157], v[214:217], v[14:17]
	v_mfma_f32_16x16x32_bf16 v[10:13], v[158:161], v[214:217], v[10:13]
	v_mfma_f32_16x16x32_bf16 v[6:9], v[154:157], v[218:221], v[6:9]
	v_mfma_f32_16x16x32_bf16 v[2:5], v[158:161], v[218:221], v[2:5]
	s_setprio 0
	s_barrier
	s_add_i32 s62, 0, 0x18000
	v_add_u32_e32 v174, s62, v201
	v_add_u32_e32 v175, s62, v202
	s_add_i32 s62, 0, 0x1c000
	v_add_u32_e32 v176, s62, v201
	ds_read_b128 v[130:133], v174
	ds_read_b128 v[134:137], v174 offset:2048
	ds_read_b128 v[138:141], v175
	ds_read_b128 v[142:145], v175 offset:2048
	v_add_u32_e32 v177, s62, v202
	ds_read_b128 v[146:149], v176
	ds_read_b128 v[150:153], v176 offset:2048
	ds_read_b128 v[154:157], v177
	ds_read_b128 v[158:161], v177 offset:2048
	ds_read_b128 v[162:165], v207 offset:32768
	ds_read_b128 v[166:169], v207 offset:34816
	ds_read_b128 v[178:181], v208 offset:32768
	ds_read_b128 v[182:185], v208 offset:34816
	ds_read_b128 v[210:213], v207 offset:36864
	ds_read_b128 v[214:217], v207 offset:38912
	ds_read_b128 v[218:221], v208 offset:36864
	ds_read_b128 v[222:225], v208 offset:38912
	s_mov_b32 m0, s44
	s_nop 0
	global_load_lds_dwordx4 v198, s[58:59] offset:0
	s_nop 0
	s_mov_b32 m0, s45
	s_nop 0
	global_load_lds_dwordx4 v200, s[58:59] offset:0
	s_waitcnt vmcnt(8)
	s_waitcnt lgkmcnt(0)
	s_barrier
	s_setprio 1
	s_waitcnt lgkmcnt(7)
	v_mfma_f32_16x16x32_bf16 v[126:129], v[130:133], v[162:165], v[126:129]
	v_mfma_f32_16x16x32_bf16 v[122:125], v[134:137], v[162:165], v[122:125]
	s_waitcnt lgkmcnt(6)
	v_mfma_f32_16x16x32_bf16 v[118:121], v[130:133], v[166:169], v[118:121]
	v_mfma_f32_16x16x32_bf16 v[114:117], v[134:137], v[166:169], v[114:117]
	s_waitcnt lgkmcnt(3)
	v_mfma_f32_16x16x32_bf16 v[110:113], v[130:133], v[210:213], v[110:113]
	v_mfma_f32_16x16x32_bf16 v[106:109], v[134:137], v[210:213], v[106:109]
	s_waitcnt lgkmcnt(2)
	v_mfma_f32_16x16x32_bf16 v[102:105], v[130:133], v[214:217], v[102:105]
	v_mfma_f32_16x16x32_bf16 v[98:101], v[134:137], v[214:217], v[98:101]
	v_mfma_f32_16x16x32_bf16 v[126:129], v[138:141], v[178:181], v[126:129]
	v_mfma_f32_16x16x32_bf16 v[122:125], v[142:145], v[178:181], v[122:125]
	v_mfma_f32_16x16x32_bf16 v[118:121], v[138:141], v[182:185], v[118:121]
	v_mfma_f32_16x16x32_bf16 v[114:117], v[142:145], v[182:185], v[114:117]
	s_waitcnt lgkmcnt(1)
	v_mfma_f32_16x16x32_bf16 v[110:113], v[138:141], v[218:221], v[110:113]
	v_mfma_f32_16x16x32_bf16 v[106:109], v[142:145], v[218:221], v[106:109]
	s_waitcnt lgkmcnt(0)
	v_mfma_f32_16x16x32_bf16 v[102:105], v[138:141], v[222:225], v[102:105]
	v_mfma_f32_16x16x32_bf16 v[98:101], v[142:145], v[222:225], v[98:101]
	s_setprio 0
	s_setprio 1
	v_mfma_f32_16x16x32_bf16 v[94:97], v[146:149], v[162:165], v[94:97]
	v_mfma_f32_16x16x32_bf16 v[90:93], v[150:153], v[162:165], v[90:93]
	v_mfma_f32_16x16x32_bf16 v[86:89], v[146:149], v[166:169], v[86:89]
	v_mfma_f32_16x16x32_bf16 v[82:85], v[150:153], v[166:169], v[82:85]
	v_mfma_f32_16x16x32_bf16 v[78:81], v[146:149], v[210:213], v[78:81]
	v_mfma_f32_16x16x32_bf16 v[74:77], v[150:153], v[210:213], v[74:77]
	v_mfma_f32_16x16x32_bf16 v[70:73], v[146:149], v[214:217], v[70:73]
	v_mfma_f32_16x16x32_bf16 v[66:69], v[150:153], v[214:217], v[66:69]
	v_mfma_f32_16x16x32_bf16 v[94:97], v[154:157], v[178:181], v[94:97]
	v_mfma_f32_16x16x32_bf16 v[90:93], v[158:161], v[178:181], v[90:93]
	v_mfma_f32_16x16x32_bf16 v[86:89], v[154:157], v[182:185], v[86:89]
	v_mfma_f32_16x16x32_bf16 v[82:85], v[158:161], v[182:185], v[82:85]
	v_mfma_f32_16x16x32_bf16 v[78:81], v[154:157], v[218:221], v[78:81]
	v_mfma_f32_16x16x32_bf16 v[74:77], v[158:161], v[218:221], v[74:77]
	v_mfma_f32_16x16x32_bf16 v[70:73], v[154:157], v[222:225], v[70:73]
	v_mfma_f32_16x16x32_bf16 v[66:69], v[158:161], v[222:225], v[66:69]
	s_setprio 0
	s_barrier
	ds_read_b128 v[162:165], v207 offset:49152
	ds_read_b128 v[166:169], v207 offset:51200
	ds_read_b128 v[178:181], v208 offset:49152
	ds_read_b128 v[182:185], v208 offset:51200
	ds_read_b128 v[210:213], v207 offset:53248
	ds_read_b128 v[214:217], v207 offset:55296
	ds_read_b128 v[218:221], v208 offset:53248
	ds_read_b128 v[222:225], v208 offset:55296
	s_add_u32 s58, s60, 0x180
	s_addc_u32 s59, s61, 0
	s_mov_b32 m0, s46
	s_nop 0
	global_load_lds_dwordx4 v195, s[58:59] offset:0
	s_nop 0
	s_mov_b32 m0, s47
	s_nop 0
	global_load_lds_dwordx4 v196, s[58:59] offset:0
	s_add_u32 s58, s60, 0x40180
	s_addc_u32 s59, s61, 0
	s_mov_b32 m0, s50
	s_nop 0
	global_load_lds_dwordx4 v195, s[58:59] offset:0
	s_add_u32 s36, s36, 0x180
	s_mov_b32 m0, s51
	s_nop 0
	global_load_lds_dwordx4 v196, s[58:59] offset:0
	s_addc_u32 s37, s37, 0
	s_mov_b32 m0, s48
	s_nop 0
	global_load_lds_dwordx4 v197, s[36:37] offset:0
	s_nop 0
	s_mov_b32 m0, s49
	s_nop 0
	global_load_lds_dwordx4 v199, s[36:37] offset:0
	s_waitcnt vmcnt(8)
	s_waitcnt lgkmcnt(0)
	s_barrier
	s_setprio 1
	s_waitcnt lgkmcnt(7)
	v_mfma_f32_16x16x32_bf16 v[62:65], v[130:133], v[162:165], v[62:65]
	v_mfma_f32_16x16x32_bf16 v[58:61], v[134:137], v[162:165], v[58:61]
	s_waitcnt lgkmcnt(6)
	v_mfma_f32_16x16x32_bf16 v[54:57], v[130:133], v[166:169], v[54:57]
	v_mfma_f32_16x16x32_bf16 v[50:53], v[134:137], v[166:169], v[50:53]
	s_waitcnt lgkmcnt(3)
	v_mfma_f32_16x16x32_bf16 v[46:49], v[130:133], v[210:213], v[46:49]
	v_mfma_f32_16x16x32_bf16 v[42:45], v[134:137], v[210:213], v[42:45]
	s_waitcnt lgkmcnt(2)
	v_mfma_f32_16x16x32_bf16 v[38:41], v[130:133], v[214:217], v[38:41]
	v_mfma_f32_16x16x32_bf16 v[34:37], v[134:137], v[214:217], v[34:37]
	v_mfma_f32_16x16x32_bf16 v[62:65], v[138:141], v[178:181], v[62:65]
	v_mfma_f32_16x16x32_bf16 v[58:61], v[142:145], v[178:181], v[58:61]
	v_mfma_f32_16x16x32_bf16 v[54:57], v[138:141], v[182:185], v[54:57]
	v_mfma_f32_16x16x32_bf16 v[50:53], v[142:145], v[182:185], v[50:53]
	s_waitcnt lgkmcnt(1)
	v_mfma_f32_16x16x32_bf16 v[46:49], v[138:141], v[218:221], v[46:49]
	v_mfma_f32_16x16x32_bf16 v[42:45], v[142:145], v[218:221], v[42:45]
	s_waitcnt lgkmcnt(0)
	v_mfma_f32_16x16x32_bf16 v[38:41], v[138:141], v[222:225], v[38:41]
	v_mfma_f32_16x16x32_bf16 v[34:37], v[142:145], v[222:225], v[34:37]
	s_setprio 0
	s_setprio 1
	v_mfma_f32_16x16x32_bf16 v[30:33], v[146:149], v[162:165], v[30:33]
	v_mfma_f32_16x16x32_bf16 v[26:29], v[150:153], v[162:165], v[26:29]
	v_mfma_f32_16x16x32_bf16 v[22:25], v[146:149], v[166:169], v[22:25]
	v_mfma_f32_16x16x32_bf16 v[18:21], v[150:153], v[166:169], v[18:21]
	v_mfma_f32_16x16x32_bf16 v[14:17], v[146:149], v[210:213], v[14:17]
	v_mfma_f32_16x16x32_bf16 v[10:13], v[150:153], v[210:213], v[10:13]
	v_mfma_f32_16x16x32_bf16 v[6:9], v[146:149], v[214:217], v[6:9]
	v_mfma_f32_16x16x32_bf16 v[2:5], v[150:153], v[214:217], v[2:5]
	v_mfma_f32_16x16x32_bf16 v[30:33], v[154:157], v[178:181], v[30:33]
	v_mfma_f32_16x16x32_bf16 v[26:29], v[158:161], v[178:181], v[26:29]
	v_mfma_f32_16x16x32_bf16 v[22:25], v[154:157], v[182:185], v[22:25]
	v_mfma_f32_16x16x32_bf16 v[18:21], v[158:161], v[182:185], v[18:21]
	v_mfma_f32_16x16x32_bf16 v[14:17], v[154:157], v[218:221], v[14:17]
	v_mfma_f32_16x16x32_bf16 v[10:13], v[158:161], v[218:221], v[10:13]
	v_mfma_f32_16x16x32_bf16 v[6:9], v[154:157], v[222:225], v[6:9]
	v_mfma_f32_16x16x32_bf16 v[2:5], v[158:161], v[222:225], v[2:5]
	s_setprio 0
	s_add_i32 s31, s31, 2
	s_add_u32 s6, s6, 0x100
	s_addc_u32 s7, s7, 0
	s_cmp_lt_u32 s31, 12
	s_barrier
	s_cbranch_scc1 .LBB0_368
	ds_read_b128 v[154:157], v203
	ds_read_b128 v[158:161], v203 offset:2048
	ds_read_b128 v[166:169], v204
	ds_read_b128 v[162:165], v204 offset:2048
	ds_read_b128 v[138:141], v205
	ds_read_b128 v[142:145], v205 offset:2048
	ds_read_b128 v[150:153], v206
	ds_read_b128 v[146:149], v206 offset:2048
	ds_read_b128 v[134:137], v207
	ds_read_b128 v[178:181], v207 offset:2048
	ds_read_b128 v[182:185], v208
	ds_read_b128 v[210:213], v208 offset:2048
	ds_read_b128 v[214:217], v207 offset:4096
	ds_read_b128 v[218:221], v207 offset:6144
	ds_read_b128 v[222:225], v208 offset:4096
	ds_read_b128 v[226:229], v208 offset:6144
	s_mov_b32 m0, s52
	s_nop 0
	global_load_lds_dwordx4 v198, s[20:21] offset:0
	s_nop 0
	s_mov_b32 m0, s53
	s_nop 0
	global_load_lds_dwordx4 v200, s[20:21] offset:0
	s_waitcnt vmcnt(8)
	s_waitcnt lgkmcnt(0)
	s_barrier
	s_setprio 1
	s_waitcnt lgkmcnt(7)
	v_mfma_f32_16x16x32_bf16 v[126:129], v[154:157], v[134:137], v[126:129]
	v_mfma_f32_16x16x32_bf16 v[122:125], v[158:161], v[134:137], v[122:125]
	s_waitcnt lgkmcnt(6)
	v_mfma_f32_16x16x32_bf16 v[118:121], v[154:157], v[178:181], v[118:121]
	v_mfma_f32_16x16x32_bf16 v[114:117], v[158:161], v[178:181], v[114:117]
	s_waitcnt lgkmcnt(3)
	v_mfma_f32_16x16x32_bf16 v[110:113], v[154:157], v[214:217], v[110:113]
	v_mfma_f32_16x16x32_bf16 v[106:109], v[158:161], v[214:217], v[106:109]
	s_waitcnt lgkmcnt(2)
	v_mfma_f32_16x16x32_bf16 v[102:105], v[154:157], v[218:221], v[102:105]
	v_mfma_f32_16x16x32_bf16 v[98:101], v[158:161], v[218:221], v[98:101]
	v_mfma_f32_16x16x32_bf16 v[126:129], v[166:169], v[182:185], v[126:129]
	v_mfma_f32_16x16x32_bf16 v[122:125], v[162:165], v[182:185], v[122:125]
	v_mfma_f32_16x16x32_bf16 v[118:121], v[166:169], v[210:213], v[118:121]
	v_mfma_f32_16x16x32_bf16 v[114:117], v[162:165], v[210:213], v[114:117]
	s_waitcnt lgkmcnt(1)
	v_mfma_f32_16x16x32_bf16 v[110:113], v[166:169], v[222:225], v[110:113]
	v_mfma_f32_16x16x32_bf16 v[106:109], v[162:165], v[222:225], v[106:109]
	s_waitcnt lgkmcnt(0)
	v_mfma_f32_16x16x32_bf16 v[102:105], v[166:169], v[226:229], v[102:105]
	v_mfma_f32_16x16x32_bf16 v[98:101], v[162:165], v[226:229], v[98:101]
	s_setprio 0
	s_setprio 1
	v_mfma_f32_16x16x32_bf16 v[94:97], v[138:141], v[134:137], v[94:97]
	v_mfma_f32_16x16x32_bf16 v[90:93], v[142:145], v[134:137], v[90:93]
	v_mfma_f32_16x16x32_bf16 v[86:89], v[138:141], v[178:181], v[86:89]
	v_mfma_f32_16x16x32_bf16 v[82:85], v[142:145], v[178:181], v[82:85]
	v_mfma_f32_16x16x32_bf16 v[78:81], v[138:141], v[214:217], v[78:81]
	v_mfma_f32_16x16x32_bf16 v[74:77], v[142:145], v[214:217], v[74:77]
	v_mfma_f32_16x16x32_bf16 v[70:73], v[138:141], v[218:221], v[70:73]
	v_mfma_f32_16x16x32_bf16 v[66:69], v[142:145], v[218:221], v[66:69]
	v_mfma_f32_16x16x32_bf16 v[130:133], v[150:153], v[182:185], v[94:97]
	v_mfma_f32_16x16x32_bf16 v[134:137], v[146:149], v[182:185], v[90:93]
	v_mfma_f32_16x16x32_bf16 v[86:89], v[150:153], v[210:213], v[86:89]
	v_mfma_f32_16x16x32_bf16 v[82:85], v[146:149], v[210:213], v[82:85]
	v_mfma_f32_16x16x32_bf16 v[78:81], v[150:153], v[222:225], v[78:81]
	v_mfma_f32_16x16x32_bf16 v[74:77], v[146:149], v[222:225], v[74:77]
	v_mfma_f32_16x16x32_bf16 v[70:73], v[150:153], v[226:229], v[70:73]
	v_mfma_f32_16x16x32_bf16 v[66:69], v[146:149], v[226:229], v[66:69]
	s_setprio 0
	s_barrier
	v_cndmask_b32_e64 v90, 0, 1, s[4:5]
	v_cmp_ne_u32_e64 s[6:7], 1, v90
	s_andn2_b64 vcc, exec, s[4:5]
	s_cbranch_vccnz .LBB0_371
	v_mov_b32_e32 v90, v0
	s_nop 0
	v_lshlrev_b32_e32 v91, 4, v90
	v_bitop3_b32 v91, v91, s3, v90 bitop3:0x48
	v_lshlrev_b32_e32 v90, 8, v90
	v_lshl_or_b32 v91, s55, 19, v91
	v_and_b32_e32 v90, 0xfffff800, v90
	v_add_u32_e32 v197, v91, v90
	v_add_u32_e32 v198, 0x40000, v197
	v_add_u32_e32 v199, 0x20000, v197
	v_add_u32_e32 v200, 0x60000, v197

.LBB0_560:
	s_mov_b32 s35, -2
	.p2align 5
	s_nop 0
	ds_read_b128 v[18:21], v179
	ds_read_b128 v[26:29], v179 offset:2048
	ds_read_b128 v[22:25], v180
	ds_read_b128 v[30:33], v180 offset:2048
	ds_read_b128 v[2:5], v181
	ds_read_b128 v[10:13], v181 offset:2048
	ds_read_b128 v[6:9], v182
	ds_read_b128 v[14:17], v182 offset:2048
	ds_read_b128 v[194:197], v183
	ds_read_b128 v[202:205], v183 offset:2048
	ds_read_b128 v[198:201], v184
	ds_read_b128 v[206:209], v184 offset:2048
	ds_read_b128 v[210:213], v183 offset:4096
	ds_read_b128 v[218:221], v183 offset:6144
	ds_read_b128 v[214:217], v184 offset:4096
	ds_read_b128 v[222:225], v184 offset:6144
	s_add_u32 s39, s18, s4
	s_addc_u32 s68, s19, s5
	s_add_u32 s42, s39, 0x80
	s_addc_u32 s43, s68, 0
	s_mov_b32 m0, s61
	s_nop 0
	global_load_lds_dwordx4 v172, s[42:43] offset:0
	s_nop 0
	s_mov_b32 m0, s62
	s_nop 0
	global_load_lds_dwordx4 v175, s[42:43] offset:0
	s_waitcnt vmcnt(8)
	s_waitcnt lgkmcnt(0)
	s_barrier
	s_setprio 1
	s_waitcnt lgkmcnt(5)
	v_mfma_f32_16x16x128_f8f6f4 v[158:161], v[18:25], v[194:201], 0
	v_mfma_f32_16x16x128_f8f6f4 v[150:153], v[26:33], v[194:201], 0
	s_waitcnt lgkmcnt(4)
	v_mfma_f32_16x16x128_f8f6f4 v[142:145], v[18:25], v[202:209], 0
	v_mfma_f32_16x16x128_f8f6f4 v[134:137], v[26:33], v[202:209], 0
	s_waitcnt lgkmcnt(1)
	v_mfma_f32_16x16x128_f8f6f4 v[126:129], v[18:25], v[210:217], 0
	v_mfma_f32_16x16x128_f8f6f4 v[118:121], v[26:33], v[210:217], 0
	s_waitcnt lgkmcnt(0)
	v_mfma_f32_16x16x128_f8f6f4 v[110:113], v[18:25], v[218:225], 0
	v_mfma_f32_16x16x128_f8f6f4 v[102:105], v[26:33], v[218:225], 0
	s_setprio 0
	s_setprio 1
	v_mfma_f32_16x16x128_f8f6f4 v[154:157], v[2:9], v[194:201], 0
	v_mfma_f32_16x16x128_f8f6f4 v[146:149], v[10:17], v[194:201], 0
	v_mfma_f32_16x16x128_f8f6f4 v[138:141], v[2:9], v[202:209], 0
	v_mfma_f32_16x16x128_f8f6f4 v[130:133], v[10:17], v[202:209], 0
	v_mfma_f32_16x16x128_f8f6f4 v[122:125], v[2:9], v[210:217], 0
	v_mfma_f32_16x16x128_f8f6f4 v[114:117], v[10:17], v[210:217], 0
	v_mfma_f32_16x16x128_f8f6f4 v[106:109], v[2:9], v[218:225], 0
	v_mfma_f32_16x16x128_f8f6f4 v[98:101], v[10:17], v[218:225], 0
	s_setprio 0
	s_barrier
	s_add_u32 s69, s44, s4
	s_addc_u32 s70, s45, s5
	ds_read_b128 v[194:197], v183 offset:16384
	ds_read_b128 v[202:205], v183 offset:18432
	ds_read_b128 v[198:201], v184 offset:16384
	ds_read_b128 v[206:209], v184 offset:18432
	ds_read_b128 v[210:213], v183 offset:20480
	ds_read_b128 v[218:221], v183 offset:22528
	ds_read_b128 v[214:217], v184 offset:20480
	ds_read_b128 v[222:225], v184 offset:22528
	s_add_u32 s42, s69, 0x100
	s_addc_u32 s43, s70, 0
	s_mov_b32 m0, s48
	s_nop 0
	global_load_lds_dwordx4 v1, s[42:43] offset:0
	s_nop 0
	s_mov_b32 m0, s49
	s_nop 0
	global_load_lds_dwordx4 v173, s[42:43] offset:0
	s_add_u32 s42, s69, 0x20100
	s_addc_u32 s43, s70, 0
	s_mov_b32 m0, s50
	s_nop 0
	global_load_lds_dwordx4 v1, s[42:43] offset:0
	s_nop 0
	s_mov_b32 m0, s51
	s_nop 0
	global_load_lds_dwordx4 v173, s[42:43] offset:0
	s_add_u32 s42, s39, 0x100
	s_addc_u32 s43, s68, 0
	s_mov_b32 m0, s29
	s_nop 0
	global_load_lds_dwordx4 v171, s[42:43] offset:0
	s_nop 0
	s_mov_b32 m0, s52
	s_nop 0
	global_load_lds_dwordx4 v174, s[42:43] offset:0
	s_waitcnt vmcnt(8)
	s_waitcnt lgkmcnt(0)
	s_barrier
	s_setprio 1
	s_waitcnt lgkmcnt(5)
	v_mfma_f32_16x16x128_f8f6f4 v[94:97], v[18:25], v[194:201], 0
	v_mfma_f32_16x16x128_f8f6f4 v[86:89], v[26:33], v[194:201], 0
	s_waitcnt lgkmcnt(4)
	v_mfma_f32_16x16x128_f8f6f4 v[78:81], v[18:25], v[202:209], 0
	v_mfma_f32_16x16x128_f8f6f4 v[70:73], v[26:33], v[202:209], 0
	s_waitcnt lgkmcnt(1)
	v_mfma_f32_16x16x128_f8f6f4 v[62:65], v[18:25], v[210:217], 0
	v_mfma_f32_16x16x128_f8f6f4 v[54:57], v[26:33], v[210:217], 0
	s_waitcnt lgkmcnt(0)
	v_mfma_f32_16x16x128_f8f6f4 v[46:49], v[18:25], v[218:225], 0
	v_mfma_f32_16x16x128_f8f6f4 v[38:41], v[26:33], v[218:225], 0
	s_setprio 0
	s_setprio 1
	v_mfma_f32_16x16x128_f8f6f4 v[90:93], v[2:9], v[194:201], 0
	v_mfma_f32_16x16x128_f8f6f4 v[82:85], v[10:17], v[194:201], 0
	v_mfma_f32_16x16x128_f8f6f4 v[74:77], v[2:9], v[202:209], 0
	v_mfma_f32_16x16x128_f8f6f4 v[66:69], v[10:17], v[202:209], 0
	v_mfma_f32_16x16x128_f8f6f4 v[58:61], v[2:9], v[210:217], 0
	v_mfma_f32_16x16x128_f8f6f4 v[50:53], v[10:17], v[210:217], 0
	v_mfma_f32_16x16x128_f8f6f4 v[42:45], v[2:9], v[218:225], 0
	v_mfma_f32_16x16x128_f8f6f4 v[34:37], v[10:17], v[218:225], 0
	s_setprio 0
	s_barrier
	s_add_i32 s71, 0, 0x18000
	v_add_u32_e32 v162, s71, v176
	v_add_u32_e32 v187, s71, v177
	s_add_i32 s71, 0, 0x1c000
	v_add_u32_e32 v194, s71, v176
	ds_read_b128 v[2:5], v162
	ds_read_b128 v[10:13], v162 offset:2048
	ds_read_b128 v[6:9], v187
	ds_read_b128 v[14:17], v187 offset:2048
	v_add_u32_e32 v195, s71, v177
	ds_read_b128 v[18:21], v194
	ds_read_b128 v[26:29], v194 offset:2048
	ds_read_b128 v[22:25], v195
	ds_read_b128 v[30:33], v195 offset:2048
	ds_read_b128 v[196:199], v183 offset:32768
	ds_read_b128 v[204:207], v183 offset:34816
	ds_read_b128 v[200:203], v184 offset:32768
	ds_read_b128 v[208:211], v184 offset:34816
	ds_read_b128 v[212:215], v183 offset:36864
	ds_read_b128 v[220:223], v183 offset:38912
	ds_read_b128 v[216:219], v184 offset:36864
	ds_read_b128 v[224:227], v184 offset:38912
	s_mov_b32 m0, s53
	s_nop 0
	global_load_lds_dwordx4 v172, s[42:43] offset:0
	s_nop 0
	s_mov_b32 m0, s54
	s_nop 0
	global_load_lds_dwordx4 v175, s[42:43] offset:0
	s_waitcnt vmcnt(8)
	s_waitcnt lgkmcnt(0)
	s_barrier
	s_setprio 1
	s_waitcnt lgkmcnt(5)
	v_mfma_f32_16x16x128_f8f6f4 v[158:161], v[2:9], v[196:203], v[158:161]
	v_mfma_f32_16x16x128_f8f6f4 v[150:153], v[10:17], v[196:203], v[150:153]
	s_waitcnt lgkmcnt(4)
	v_mfma_f32_16x16x128_f8f6f4 v[142:145], v[2:9], v[204:211], v[142:145]
	v_mfma_f32_16x16x128_f8f6f4 v[134:137], v[10:17], v[204:211], v[134:137]
	s_waitcnt lgkmcnt(1)
	v_mfma_f32_16x16x128_f8f6f4 v[126:129], v[2:9], v[212:219], v[126:129]
	v_mfma_f32_16x16x128_f8f6f4 v[118:121], v[10:17], v[212:219], v[118:121]
	s_waitcnt lgkmcnt(0)
	v_mfma_f32_16x16x128_f8f6f4 v[110:113], v[2:9], v[220:227], v[110:113]
	v_mfma_f32_16x16x128_f8f6f4 v[102:105], v[10:17], v[220:227], v[102:105]
	s_setprio 0
	s_setprio 1
	v_mfma_f32_16x16x128_f8f6f4 v[154:157], v[18:25], v[196:203], v[154:157]
	v_mfma_f32_16x16x128_f8f6f4 v[146:149], v[26:33], v[196:203], v[146:149]
	v_mfma_f32_16x16x128_f8f6f4 v[138:141], v[18:25], v[204:211], v[138:141]
	v_mfma_f32_16x16x128_f8f6f4 v[130:133], v[26:33], v[204:211], v[130:133]
	v_mfma_f32_16x16x128_f8f6f4 v[122:125], v[18:25], v[212:219], v[122:125]
	v_mfma_f32_16x16x128_f8f6f4 v[114:117], v[26:33], v[212:219], v[114:117]
	v_mfma_f32_16x16x128_f8f6f4 v[106:109], v[18:25], v[220:227], v[106:109]
	v_mfma_f32_16x16x128_f8f6f4 v[98:101], v[26:33], v[220:227], v[98:101]
	s_setprio 0
	s_barrier
	ds_read_b128 v[196:199], v183 offset:49152
	ds_read_b128 v[204:207], v183 offset:51200
	ds_read_b128 v[200:203], v184 offset:49152
	ds_read_b128 v[208:211], v184 offset:51200
	ds_read_b128 v[212:215], v183 offset:53248
	ds_read_b128 v[220:223], v183 offset:55296
	ds_read_b128 v[216:219], v184 offset:53248
	ds_read_b128 v[224:227], v184 offset:55296
	s_add_u32 s42, s69, 0x180
	s_addc_u32 s43, s70, 0
	s_mov_b32 m0, s55
	s_nop 0
	global_load_lds_dwordx4 v1, s[42:43] offset:0
	s_nop 0
	s_mov_b32 m0, s56
	s_nop 0
	global_load_lds_dwordx4 v173, s[42:43] offset:0
	s_add_u32 s42, s69, 0x20180
	s_addc_u32 s43, s70, 0
	s_mov_b32 m0, s59
	s_nop 0
	global_load_lds_dwordx4 v1, s[42:43] offset:0
	s_nop 0
	s_mov_b32 m0, s60
	s_nop 0
	global_load_lds_dwordx4 v173, s[42:43] offset:0
	s_add_u32 s42, s39, 0x180
	s_addc_u32 s43, s68, 0
	s_mov_b32 m0, s57
	s_nop 0
	global_load_lds_dwordx4 v171, s[42:43] offset:0
	s_nop 0
	s_mov_b32 m0, s58
	s_nop 0
	global_load_lds_dwordx4 v174, s[42:43] offset:0
	s_waitcnt vmcnt(8)
	s_waitcnt lgkmcnt(0)
	s_barrier
	s_setprio 1
	s_waitcnt lgkmcnt(5)
	v_mfma_f32_16x16x128_f8f6f4 v[94:97], v[2:9], v[196:203], v[94:97]
	v_mfma_f32_16x16x128_f8f6f4 v[86:89], v[10:17], v[196:203], v[86:89]
	s_waitcnt lgkmcnt(4)
	v_mfma_f32_16x16x128_f8f6f4 v[78:81], v[2:9], v[204:211], v[78:81]
	v_mfma_f32_16x16x128_f8f6f4 v[70:73], v[10:17], v[204:211], v[70:73]
	s_waitcnt lgkmcnt(1)
	v_mfma_f32_16x16x128_f8f6f4 v[62:65], v[2:9], v[212:219], v[62:65]
	v_mfma_f32_16x16x128_f8f6f4 v[54:57], v[10:17], v[212:219], v[54:57]
	s_waitcnt lgkmcnt(0)
	v_mfma_f32_16x16x128_f8f6f4 v[46:49], v[2:9], v[220:227], v[46:49]
	v_mfma_f32_16x16x128_f8f6f4 v[38:41], v[10:17], v[220:227], v[38:41]
	s_setprio 0
	s_setprio 1
	v_mfma_f32_16x16x128_f8f6f4 v[90:93], v[18:25], v[196:203], v[90:93]
	v_mfma_f32_16x16x128_f8f6f4 v[82:85], v[26:33], v[196:203], v[82:85]
	v_mfma_f32_16x16x128_f8f6f4 v[74:77], v[18:25], v[204:211], v[74:77]
	v_mfma_f32_16x16x128_f8f6f4 v[66:69], v[26:33], v[204:211], v[66:69]
	v_mfma_f32_16x16x128_f8f6f4 v[58:61], v[18:25], v[212:219], v[58:61]
	v_mfma_f32_16x16x128_f8f6f4 v[50:53], v[26:33], v[212:219], v[50:53]
	v_mfma_f32_16x16x128_f8f6f4 v[42:45], v[18:25], v[220:227], v[42:45]
	v_mfma_f32_16x16x128_f8f6f4 v[34:37], v[26:33], v[220:227], v[34:37]
	s_setprio 0
	s_add_i32 s35, s35, 2
	s_add_u32 s4, s4, 0x100
	s_addc_u32 s5, s5, 0
	s_barrier
.LBB0_561:
	.p2align 5
	s_nop 0
	ds_read_b128 v[18:21], v179
	ds_read_b128 v[26:29], v179 offset:2048
	ds_read_b128 v[22:25], v180
	ds_read_b128 v[30:33], v180 offset:2048
	ds_read_b128 v[2:5], v181
	ds_read_b128 v[10:13], v181 offset:2048
	ds_read_b128 v[6:9], v182
	ds_read_b128 v[14:17], v182 offset:2048
	ds_read_b128 v[194:197], v183
	ds_read_b128 v[202:205], v183 offset:2048
	ds_read_b128 v[198:201], v184
	ds_read_b128 v[206:209], v184 offset:2048
	ds_read_b128 v[210:213], v183 offset:4096
	ds_read_b128 v[218:221], v183 offset:6144
	ds_read_b128 v[214:217], v184 offset:4096
	ds_read_b128 v[222:225], v184 offset:6144
	s_add_u32 s39, s18, s4
	s_addc_u32 s68, s19, s5
	s_add_u32 s42, s39, 0x80
	s_addc_u32 s43, s68, 0
	s_mov_b32 m0, s61
	s_nop 0
	global_load_lds_dwordx4 v172, s[42:43] offset:0
	s_nop 0
	s_mov_b32 m0, s62
	s_nop 0
	global_load_lds_dwordx4 v175, s[42:43] offset:0
	s_waitcnt vmcnt(8)
	s_waitcnt lgkmcnt(0)
	s_barrier
	s_setprio 1
	s_waitcnt lgkmcnt(5)
	v_mfma_f32_16x16x128_f8f6f4 v[158:161], v[18:25], v[194:201], v[158:161]
	v_mfma_f32_16x16x128_f8f6f4 v[150:153], v[26:33], v[194:201], v[150:153]
	s_waitcnt lgkmcnt(4)
	v_mfma_f32_16x16x128_f8f6f4 v[142:145], v[18:25], v[202:209], v[142:145]
	v_mfma_f32_16x16x128_f8f6f4 v[134:137], v[26:33], v[202:209], v[134:137]
	s_waitcnt lgkmcnt(1)
	v_mfma_f32_16x16x128_f8f6f4 v[126:129], v[18:25], v[210:217], v[126:129]
	v_mfma_f32_16x16x128_f8f6f4 v[118:121], v[26:33], v[210:217], v[118:121]
	s_waitcnt lgkmcnt(0)
	v_mfma_f32_16x16x128_f8f6f4 v[110:113], v[18:25], v[218:225], v[110:113]
	v_mfma_f32_16x16x128_f8f6f4 v[102:105], v[26:33], v[218:225], v[102:105]
	s_setprio 0
	s_setprio 1
	v_mfma_f32_16x16x128_f8f6f4 v[154:157], v[2:9], v[194:201], v[154:157]
	v_mfma_f32_16x16x128_f8f6f4 v[146:149], v[10:17], v[194:201], v[146:149]
	v_mfma_f32_16x16x128_f8f6f4 v[138:141], v[2:9], v[202:209], v[138:141]
	v_mfma_f32_16x16x128_f8f6f4 v[130:133], v[10:17], v[202:209], v[130:133]
	v_mfma_f32_16x16x128_f8f6f4 v[122:125], v[2:9], v[210:217], v[122:125]
	v_mfma_f32_16x16x128_f8f6f4 v[114:117], v[10:17], v[210:217], v[114:117]
	v_mfma_f32_16x16x128_f8f6f4 v[106:109], v[2:9], v[218:225], v[106:109]
	v_mfma_f32_16x16x128_f8f6f4 v[98:101], v[10:17], v[218:225], v[98:101]
	s_setprio 0
	s_barrier
	s_add_u32 s69, s44, s4
	s_addc_u32 s70, s45, s5
	ds_read_b128 v[194:197], v183 offset:16384
	ds_read_b128 v[202:205], v183 offset:18432
	ds_read_b128 v[198:201], v184 offset:16384
	ds_read_b128 v[206:209], v184 offset:18432
	ds_read_b128 v[210:213], v183 offset:20480
	ds_read_b128 v[218:221], v183 offset:22528
	ds_read_b128 v[214:217], v184 offset:20480
	ds_read_b128 v[222:225], v184 offset:22528
	s_add_u32 s42, s69, 0x100
	s_addc_u32 s43, s70, 0
	s_mov_b32 m0, s48
	s_nop 0
	global_load_lds_dwordx4 v1, s[42:43] offset:0
	s_nop 0
	s_mov_b32 m0, s49
	s_nop 0
	global_load_lds_dwordx4 v173, s[42:43] offset:0
	s_add_u32 s42, s69, 0x20100
	s_addc_u32 s43, s70, 0
	s_mov_b32 m0, s50
	s_nop 0
	global_load_lds_dwordx4 v1, s[42:43] offset:0
	s_nop 0
	s_mov_b32 m0, s51
	s_nop 0
	global_load_lds_dwordx4 v173, s[42:43] offset:0
	s_add_u32 s42, s39, 0x100
	s_addc_u32 s43, s68, 0
	s_mov_b32 m0, s29
	s_nop 0
	global_load_lds_dwordx4 v171, s[42:43] offset:0
	s_nop 0
	s_mov_b32 m0, s52
	s_nop 0
	global_load_lds_dwordx4 v174, s[42:43] offset:0
	s_waitcnt vmcnt(8)
	s_waitcnt lgkmcnt(0)
	s_barrier
	s_setprio 1
	s_waitcnt lgkmcnt(5)
	v_mfma_f32_16x16x128_f8f6f4 v[94:97], v[18:25], v[194:201], v[94:97]
	v_mfma_f32_16x16x128_f8f6f4 v[86:89], v[26:33], v[194:201], v[86:89]
	s_waitcnt lgkmcnt(4)
	v_mfma_f32_16x16x128_f8f6f4 v[78:81], v[18:25], v[202:209], v[78:81]
	v_mfma_f32_16x16x128_f8f6f4 v[70:73], v[26:33], v[202:209], v[70:73]
	s_waitcnt lgkmcnt(1)
	v_mfma_f32_16x16x128_f8f6f4 v[62:65], v[18:25], v[210:217], v[62:65]
	v_mfma_f32_16x16x128_f8f6f4 v[54:57], v[26:33], v[210:217], v[54:57]
	s_waitcnt lgkmcnt(0)
	v_mfma_f32_16x16x128_f8f6f4 v[46:49], v[18:25], v[218:225], v[46:49]
	v_mfma_f32_16x16x128_f8f6f4 v[38:41], v[26:33], v[218:225], v[38:41]
	s_setprio 0
	s_setprio 1
	v_mfma_f32_16x16x128_f8f6f4 v[90:93], v[2:9], v[194:201], v[90:93]
	v_mfma_f32_16x16x128_f8f6f4 v[82:85], v[10:17], v[194:201], v[82:85]
	v_mfma_f32_16x16x128_f8f6f4 v[74:77], v[2:9], v[202:209], v[74:77]
	v_mfma_f32_16x16x128_f8f6f4 v[66:69], v[10:17], v[202:209], v[66:69]
	v_mfma_f32_16x16x128_f8f6f4 v[58:61], v[2:9], v[210:217], v[58:61]
	v_mfma_f32_16x16x128_f8f6f4 v[50:53], v[10:17], v[210:217], v[50:53]
	v_mfma_f32_16x16x128_f8f6f4 v[42:45], v[2:9], v[218:225], v[42:45]
	v_mfma_f32_16x16x128_f8f6f4 v[34:37], v[10:17], v[218:225], v[34:37]
	s_setprio 0
	s_barrier
	s_add_i32 s71, 0, 0x18000
	v_add_u32_e32 v162, s71, v176
	v_add_u32_e32 v187, s71, v177
	s_add_i32 s71, 0, 0x1c000
	v_add_u32_e32 v194, s71, v176
	ds_read_b128 v[2:5], v162
	ds_read_b128 v[10:13], v162 offset:2048
	ds_read_b128 v[6:9], v187
	ds_read_b128 v[14:17], v187 offset:2048
	v_add_u32_e32 v195, s71, v177
	ds_read_b128 v[18:21], v194
	ds_read_b128 v[26:29], v194 offset:2048
	ds_read_b128 v[22:25], v195
	ds_read_b128 v[30:33], v195 offset:2048
	ds_read_b128 v[196:199], v183 offset:32768
	ds_read_b128 v[204:207], v183 offset:34816
	ds_read_b128 v[200:203], v184 offset:32768
	ds_read_b128 v[208:211], v184 offset:34816
	ds_read_b128 v[212:215], v183 offset:36864
	ds_read_b128 v[220:223], v183 offset:38912
	ds_read_b128 v[216:219], v184 offset:36864
	ds_read_b128 v[224:227], v184 offset:38912
	s_mov_b32 m0, s53
	s_nop 0
	global_load_lds_dwordx4 v172, s[42:43] offset:0
	s_nop 0
	s_mov_b32 m0, s54
	s_nop 0
	global_load_lds_dwordx4 v175, s[42:43] offset:0
	s_waitcnt vmcnt(8)
	s_waitcnt lgkmcnt(0)
	s_barrier
	s_setprio 1
	s_waitcnt lgkmcnt(5)
	v_mfma_f32_16x16x128_f8f6f4 v[158:161], v[2:9], v[196:203], v[158:161]
	v_mfma_f32_16x16x128_f8f6f4 v[150:153], v[10:17], v[196:203], v[150:153]
	s_waitcnt lgkmcnt(4)
	v_mfma_f32_16x16x128_f8f6f4 v[142:145], v[2:9], v[204:211], v[142:145]
	v_mfma_f32_16x16x128_f8f6f4 v[134:137], v[10:17], v[204:211], v[134:137]
	s_waitcnt lgkmcnt(1)
	v_mfma_f32_16x16x128_f8f6f4 v[126:129], v[2:9], v[212:219], v[126:129]
	v_mfma_f32_16x16x128_f8f6f4 v[118:121], v[10:17], v[212:219], v[118:121]
	s_waitcnt lgkmcnt(0)
	v_mfma_f32_16x16x128_f8f6f4 v[110:113], v[2:9], v[220:227], v[110:113]
	v_mfma_f32_16x16x128_f8f6f4 v[102:105], v[10:17], v[220:227], v[102:105]
	s_setprio 0
	s_setprio 1
	v_mfma_f32_16x16x128_f8f6f4 v[154:157], v[18:25], v[196:203], v[154:157]
	v_mfma_f32_16x16x128_f8f6f4 v[146:149], v[26:33], v[196:203], v[146:149]
	v_mfma_f32_16x16x128_f8f6f4 v[138:141], v[18:25], v[204:211], v[138:141]
	v_mfma_f32_16x16x128_f8f6f4 v[130:133], v[26:33], v[204:211], v[130:133]
	v_mfma_f32_16x16x128_f8f6f4 v[122:125], v[18:25], v[212:219], v[122:125]
	v_mfma_f32_16x16x128_f8f6f4 v[114:117], v[26:33], v[212:219], v[114:117]
	v_mfma_f32_16x16x128_f8f6f4 v[106:109], v[18:25], v[220:227], v[106:109]
	v_mfma_f32_16x16x128_f8f6f4 v[98:101], v[26:33], v[220:227], v[98:101]
	s_setprio 0
	s_barrier
	ds_read_b128 v[196:199], v183 offset:49152
	ds_read_b128 v[204:207], v183 offset:51200
	ds_read_b128 v[200:203], v184 offset:49152
	ds_read_b128 v[208:211], v184 offset:51200
	ds_read_b128 v[212:215], v183 offset:53248
	ds_read_b128 v[220:223], v183 offset:55296
	ds_read_b128 v[216:219], v184 offset:53248
	ds_read_b128 v[224:227], v184 offset:55296
	s_add_u32 s42, s69, 0x180
	s_addc_u32 s43, s70, 0
	s_mov_b32 m0, s55
	s_nop 0
	global_load_lds_dwordx4 v1, s[42:43] offset:0
	s_nop 0
	s_mov_b32 m0, s56
	s_nop 0
	global_load_lds_dwordx4 v173, s[42:43] offset:0
	s_add_u32 s42, s69, 0x20180
	s_addc_u32 s43, s70, 0
	s_mov_b32 m0, s59
	s_nop 0
	global_load_lds_dwordx4 v1, s[42:43] offset:0
	s_nop 0
	s_mov_b32 m0, s60
	s_nop 0
	global_load_lds_dwordx4 v173, s[42:43] offset:0
	s_add_u32 s42, s39, 0x180
	s_addc_u32 s43, s68, 0
	s_mov_b32 m0, s57
	s_nop 0
	global_load_lds_dwordx4 v171, s[42:43] offset:0
	s_nop 0
	s_mov_b32 m0, s58
	s_nop 0
	global_load_lds_dwordx4 v174, s[42:43] offset:0
	s_waitcnt vmcnt(8)
	s_waitcnt lgkmcnt(0)
	s_barrier
	s_setprio 1
	s_waitcnt lgkmcnt(5)
	v_mfma_f32_16x16x128_f8f6f4 v[94:97], v[2:9], v[196:203], v[94:97]
	v_mfma_f32_16x16x128_f8f6f4 v[86:89], v[10:17], v[196:203], v[86:89]
	s_waitcnt lgkmcnt(4)
	v_mfma_f32_16x16x128_f8f6f4 v[78:81], v[2:9], v[204:211], v[78:81]
	v_mfma_f32_16x16x128_f8f6f4 v[70:73], v[10:17], v[204:211], v[70:73]
	s_waitcnt lgkmcnt(1)
	v_mfma_f32_16x16x128_f8f6f4 v[62:65], v[2:9], v[212:219], v[62:65]
	v_mfma_f32_16x16x128_f8f6f4 v[54:57], v[10:17], v[212:219], v[54:57]
	s_waitcnt lgkmcnt(0)
	v_mfma_f32_16x16x128_f8f6f4 v[46:49], v[2:9], v[220:227], v[46:49]
	v_mfma_f32_16x16x128_f8f6f4 v[38:41], v[10:17], v[220:227], v[38:41]
	s_setprio 0
	s_setprio 1
	v_mfma_f32_16x16x128_f8f6f4 v[90:93], v[18:25], v[196:203], v[90:93]
	v_mfma_f32_16x16x128_f8f6f4 v[82:85], v[26:33], v[196:203], v[82:85]
	v_mfma_f32_16x16x128_f8f6f4 v[74:77], v[18:25], v[204:211], v[74:77]
	v_mfma_f32_16x16x128_f8f6f4 v[66:69], v[26:33], v[204:211], v[66:69]
	v_mfma_f32_16x16x128_f8f6f4 v[58:61], v[18:25], v[212:219], v[58:61]
	v_mfma_f32_16x16x128_f8f6f4 v[50:53], v[26:33], v[212:219], v[50:53]
	v_mfma_f32_16x16x128_f8f6f4 v[42:45], v[18:25], v[220:227], v[42:45]
	v_mfma_f32_16x16x128_f8f6f4 v[34:37], v[26:33], v[220:227], v[34:37]
	s_setprio 0
	s_add_i32 s35, s35, 2
	s_add_u32 s4, s4, 0x100
	s_addc_u32 s5, s5, 0
	s_cmp_lt_u32 s35, 4
	s_barrier
	s_cbranch_scc1 .LBB0_561
	ds_read_b128 v[18:21], v179
	ds_read_b128 v[26:29], v179 offset:2048
	ds_read_b128 v[22:25], v180
	ds_read_b128 v[30:33], v180 offset:2048
	ds_read_b128 v[2:5], v181
	ds_read_b128 v[10:13], v181 offset:2048
	ds_read_b128 v[6:9], v182
	ds_read_b128 v[14:17], v182 offset:2048
	ds_read_b128 v[196:199], v183
	ds_read_b128 v[204:207], v183 offset:2048
	ds_read_b128 v[200:203], v184
	ds_read_b128 v[208:211], v184 offset:2048
	ds_read_b128 v[212:215], v183 offset:4096
	ds_read_b128 v[220:223], v183 offset:6144
	ds_read_b128 v[216:219], v184 offset:4096
	ds_read_b128 v[224:227], v184 offset:6144
	s_mov_b32 m0, s61
	s_nop 0
	global_load_lds_dwordx4 v172, s[24:25] offset:0
	s_nop 0
	s_mov_b32 m0, s62
	s_nop 0
	global_load_lds_dwordx4 v175, s[24:25] offset:0
	s_waitcnt vmcnt(8)
	s_waitcnt lgkmcnt(0)
	s_barrier
	s_setprio 1
	s_waitcnt lgkmcnt(5)
	v_mfma_f32_16x16x128_f8f6f4 v[158:161], v[18:25], v[196:203], v[158:161]
	v_mfma_f32_16x16x128_f8f6f4 v[150:153], v[26:33], v[196:203], v[150:153]
	s_waitcnt lgkmcnt(4)
	v_mfma_f32_16x16x128_f8f6f4 v[142:145], v[18:25], v[204:211], v[142:145]
	v_mfma_f32_16x16x128_f8f6f4 v[134:137], v[26:33], v[204:211], v[134:137]
	s_waitcnt lgkmcnt(1)
	v_mfma_f32_16x16x128_f8f6f4 v[126:129], v[18:25], v[212:219], v[126:129]
	v_mfma_f32_16x16x128_f8f6f4 v[118:121], v[26:33], v[212:219], v[118:121]
	s_waitcnt lgkmcnt(0)
	v_mfma_f32_16x16x128_f8f6f4 v[110:113], v[18:25], v[220:227], v[110:113]
	v_mfma_f32_16x16x128_f8f6f4 v[102:105], v[26:33], v[220:227], v[102:105]
	s_setprio 0
	s_setprio 1
	v_mfma_f32_16x16x128_f8f6f4 v[154:157], v[2:9], v[196:203], v[154:157]
	v_mfma_f32_16x16x128_f8f6f4 v[146:149], v[10:17], v[196:203], v[146:149]
	v_mfma_f32_16x16x128_f8f6f4 v[138:141], v[2:9], v[204:211], v[138:141]
	v_mfma_f32_16x16x128_f8f6f4 v[130:133], v[10:17], v[204:211], v[130:133]
	v_mfma_f32_16x16x128_f8f6f4 v[122:125], v[2:9], v[212:219], v[122:125]
	v_mfma_f32_16x16x128_f8f6f4 v[114:117], v[10:17], v[212:219], v[114:117]
	v_mfma_f32_16x16x128_f8f6f4 v[106:109], v[2:9], v[220:227], v[106:109]
	v_mfma_f32_16x16x128_f8f6f4 v[98:101], v[10:17], v[220:227], v[98:101]
	s_setprio 0
	s_barrier
	v_cndmask_b32_e64 v196, 0, 1, s[46:47]
	v_cmp_ne_u32_e64 s[4:5], 1, v196
	s_andn2_b64 vcc, exec, s[46:47]
	s_cbranch_vccnz .LBB0_564
	v_mov_b32_e32 v171, v0
	s_lshl_b32 s35, s66, 9
	s_add_i32 s35, s35, 0
	v_lshrrev_b32_e32 v172, 4, v171
	v_xor_b32_e32 v172, v172, v171
	s_add_i32 s35, s35, 0x20480
	v_ashrrev_i32_e32 v174, 3, v171
	v_lshl_add_u32 v171, v171, 4, v170
	v_lshl_add_u32 v174, v174, 1, s35
	v_ashrrev_i32_e32 v171, 7, v171
	v_lshl_add_u32 v171, v171, 1, s35
	ds_read_u16 v175, v174
	ds_read_u16 v174, v174 offset:256
	ds_read_u16 v196, v171
	ds_read_u16 v197, v171 offset:256
	v_lshlrev_b32_e32 v172, 4, v172
	v_and_b32_e32 v198, 0x70, v172
	s_waitcnt lgkmcnt(3)
	v_lshl_or_b32 v171, v175, 10, v198
	s_waitcnt lgkmcnt(2)
	v_lshl_or_b32 v172, v174, 10, v198
	s_waitcnt lgkmcnt(1)
	v_lshl_or_b32 v174, v196, 10, v198
	s_waitcnt lgkmcnt(0)
	v_lshl_or_b32 v175, v197, 10, v198

.LBB0_649:
	s_mov_b32 s35, -2
	.p2align 5
	s_nop 0
	ds_read_b128 v[18:21], v176
	ds_read_b128 v[26:29], v176 offset:2048
	ds_read_b128 v[22:25], v177
	ds_read_b128 v[30:33], v177 offset:2048
	ds_read_b128 v[2:5], v178
	ds_read_b128 v[10:13], v178 offset:2048
	ds_read_b128 v[6:9], v179
	ds_read_b128 v[14:17], v179 offset:2048
	ds_read_b128 v[194:197], v180
	ds_read_b128 v[202:205], v180 offset:2048
	ds_read_b128 v[198:201], v181
	ds_read_b128 v[206:209], v181 offset:2048
	ds_read_b128 v[210:213], v180 offset:4096
	ds_read_b128 v[218:221], v180 offset:6144
	ds_read_b128 v[214:217], v181 offset:4096
	ds_read_b128 v[222:225], v181 offset:6144
	s_add_u32 s64, s12, s4
	s_addc_u32 s65, s13, s5
	s_add_u32 s46, s64, 0x80
	s_addc_u32 s47, s65, 0
	s_mov_b32 m0, s58
	s_nop 0
	global_load_lds_dwordx4 v163, s[46:47] offset:0
	s_nop 0
	s_mov_b32 m0, s59
	s_nop 0
	global_load_lds_dwordx4 v171, s[46:47] offset:0
	s_waitcnt vmcnt(8)
	s_waitcnt lgkmcnt(0)
	s_barrier
	s_setprio 1
	s_waitcnt lgkmcnt(0)
	v_mfma_f32_16x16x128_f8f6f4 v[158:161], v[18:25], v[194:201], 0
	v_mfma_f32_16x16x128_f8f6f4 v[154:157], v[26:33], v[194:201], 0
	v_mfma_f32_16x16x128_f8f6f4 v[142:145], v[18:25], v[202:209], 0
	v_mfma_f32_16x16x128_f8f6f4 v[138:141], v[26:33], v[202:209], 0
	v_mfma_f32_16x16x128_f8f6f4 v[126:129], v[18:25], v[210:217], 0
	v_mfma_f32_16x16x128_f8f6f4 v[122:125], v[26:33], v[210:217], 0
	v_mfma_f32_16x16x128_f8f6f4 v[110:113], v[18:25], v[218:225], 0
	v_mfma_f32_16x16x128_f8f6f4 v[106:109], v[26:33], v[218:225], 0
	s_setprio 0
	s_setprio 1
	v_mfma_f32_16x16x128_f8f6f4 v[150:153], v[2:9], v[194:201], 0
	v_mfma_f32_16x16x128_f8f6f4 v[146:149], v[10:17], v[194:201], 0
	v_mfma_f32_16x16x128_f8f6f4 v[134:137], v[2:9], v[202:209], 0
	v_mfma_f32_16x16x128_f8f6f4 v[130:133], v[10:17], v[202:209], 0
	v_mfma_f32_16x16x128_f8f6f4 v[118:121], v[2:9], v[210:217], 0
	v_mfma_f32_16x16x128_f8f6f4 v[114:117], v[10:17], v[210:217], 0
	v_mfma_f32_16x16x128_f8f6f4 v[102:105], v[2:9], v[218:225], 0
	v_mfma_f32_16x16x128_f8f6f4 v[98:101], v[10:17], v[218:225], 0
	s_setprio 0
	s_barrier
	s_add_u32 s66, s42, s4
	s_addc_u32 s67, s43, s5
	ds_read_b128 v[194:197], v180 offset:16384
	ds_read_b128 v[202:205], v180 offset:18432
	ds_read_b128 v[198:201], v181 offset:16384
	ds_read_b128 v[206:209], v181 offset:18432
	ds_read_b128 v[210:213], v180 offset:20480
	ds_read_b128 v[218:221], v180 offset:22528
	ds_read_b128 v[214:217], v181 offset:20480
	ds_read_b128 v[222:225], v181 offset:22528
	s_add_u32 s46, s66, 0x100
	s_addc_u32 s47, s67, 0
	s_mov_b32 m0, s33
	s_nop 0
	global_load_lds_dwordx4 v172, s[46:47] offset:0
	s_nop 0
	s_mov_b32 m0, s39
	s_nop 0
	global_load_lds_dwordx4 v173, s[46:47] offset:0
	s_add_u32 s46, s66, 0x20100
	s_addc_u32 s47, s67, 0
	s_mov_b32 m0, s41
	s_nop 0
	global_load_lds_dwordx4 v172, s[46:47] offset:0
	s_nop 0
	s_mov_b32 m0, s48
	s_nop 0
	global_load_lds_dwordx4 v173, s[46:47] offset:0
	s_add_u32 s46, s64, 0x100
	s_addc_u32 s47, s65, 0
	s_mov_b32 m0, s1
	s_nop 0
	global_load_lds_dwordx4 v162, s[46:47] offset:0
	s_nop 0
	s_mov_b32 m0, s49
	s_nop 0
	global_load_lds_dwordx4 v170, s[46:47] offset:0
	s_waitcnt vmcnt(8)
	s_waitcnt lgkmcnt(0)
	s_barrier
	s_setprio 1
	s_waitcnt lgkmcnt(5)
	v_mfma_f32_16x16x128_f8f6f4 v[94:97], v[18:25], v[194:201], 0
	v_mfma_f32_16x16x128_f8f6f4 v[90:93], v[26:33], v[194:201], 0
	s_waitcnt lgkmcnt(4)
	v_mfma_f32_16x16x128_f8f6f4 v[78:81], v[18:25], v[202:209], 0
	v_mfma_f32_16x16x128_f8f6f4 v[74:77], v[26:33], v[202:209], 0
	s_waitcnt lgkmcnt(1)
	v_mfma_f32_16x16x128_f8f6f4 v[62:65], v[18:25], v[210:217], 0
	v_mfma_f32_16x16x128_f8f6f4 v[58:61], v[26:33], v[210:217], 0
	s_waitcnt lgkmcnt(0)
	v_mfma_f32_16x16x128_f8f6f4 v[46:49], v[18:25], v[218:225], 0
	v_mfma_f32_16x16x128_f8f6f4 v[42:45], v[26:33], v[218:225], 0
	s_setprio 0
	s_setprio 1
	v_mfma_f32_16x16x128_f8f6f4 v[86:89], v[2:9], v[194:201], 0
	v_mfma_f32_16x16x128_f8f6f4 v[82:85], v[10:17], v[194:201], 0
	v_mfma_f32_16x16x128_f8f6f4 v[70:73], v[2:9], v[202:209], 0
	v_mfma_f32_16x16x128_f8f6f4 v[66:69], v[10:17], v[202:209], 0
	v_mfma_f32_16x16x128_f8f6f4 v[54:57], v[2:9], v[210:217], 0
	v_mfma_f32_16x16x128_f8f6f4 v[50:53], v[10:17], v[210:217], 0
	v_mfma_f32_16x16x128_f8f6f4 v[38:41], v[2:9], v[218:225], 0
	v_mfma_f32_16x16x128_f8f6f4 v[34:37], v[10:17], v[218:225], 0
	s_setprio 0
	s_barrier
	s_add_i32 s68, 0, 0x18000
	v_add_u32_e32 v183, s68, v174
	v_add_u32_e32 v184, s68, v175
	s_add_i32 s68, 0, 0x1c000
	v_add_u32_e32 v185, s68, v174
	ds_read_b128 v[2:5], v183
	ds_read_b128 v[10:13], v183 offset:2048
	ds_read_b128 v[6:9], v184
	ds_read_b128 v[14:17], v184 offset:2048
	v_add_u32_e32 v186, s68, v175
	ds_read_b128 v[18:21], v185
	ds_read_b128 v[26:29], v185 offset:2048
	ds_read_b128 v[22:25], v186
	ds_read_b128 v[30:33], v186 offset:2048
	ds_read_b128 v[194:197], v180 offset:32768
	ds_read_b128 v[202:205], v180 offset:34816
	ds_read_b128 v[198:201], v181 offset:32768
	ds_read_b128 v[206:209], v181 offset:34816
	ds_read_b128 v[210:213], v180 offset:36864
	ds_read_b128 v[218:221], v180 offset:38912
	ds_read_b128 v[214:217], v181 offset:36864
	ds_read_b128 v[222:225], v181 offset:38912
	s_mov_b32 m0, s50
	s_nop 0
	global_load_lds_dwordx4 v163, s[46:47] offset:0
	s_nop 0
	s_mov_b32 m0, s51
	s_nop 0
	global_load_lds_dwordx4 v171, s[46:47] offset:0
	s_waitcnt vmcnt(8)
	s_waitcnt lgkmcnt(0)
	s_barrier
	s_setprio 1
	s_waitcnt lgkmcnt(5)
	v_mfma_f32_16x16x128_f8f6f4 v[158:161], v[2:9], v[194:201], v[158:161]
	v_mfma_f32_16x16x128_f8f6f4 v[154:157], v[10:17], v[194:201], v[154:157]
	s_waitcnt lgkmcnt(4)
	v_mfma_f32_16x16x128_f8f6f4 v[142:145], v[2:9], v[202:209], v[142:145]
	v_mfma_f32_16x16x128_f8f6f4 v[138:141], v[10:17], v[202:209], v[138:141]
	s_waitcnt lgkmcnt(1)
	v_mfma_f32_16x16x128_f8f6f4 v[126:129], v[2:9], v[210:217], v[126:129]
	v_mfma_f32_16x16x128_f8f6f4 v[122:125], v[10:17], v[210:217], v[122:125]
	s_waitcnt lgkmcnt(0)
	v_mfma_f32_16x16x128_f8f6f4 v[110:113], v[2:9], v[218:225], v[110:113]
	v_mfma_f32_16x16x128_f8f6f4 v[106:109], v[10:17], v[218:225], v[106:109]
	s_setprio 0
	s_setprio 1
	v_mfma_f32_16x16x128_f8f6f4 v[150:153], v[18:25], v[194:201], v[150:153]
	v_mfma_f32_16x16x128_f8f6f4 v[146:149], v[26:33], v[194:201], v[146:149]
	v_mfma_f32_16x16x128_f8f6f4 v[134:137], v[18:25], v[202:209], v[134:137]
	v_mfma_f32_16x16x128_f8f6f4 v[130:133], v[26:33], v[202:209], v[130:133]
	v_mfma_f32_16x16x128_f8f6f4 v[118:121], v[18:25], v[210:217], v[118:121]
	v_mfma_f32_16x16x128_f8f6f4 v[114:117], v[26:33], v[210:217], v[114:117]
	v_mfma_f32_16x16x128_f8f6f4 v[102:105], v[18:25], v[218:225], v[102:105]
	v_mfma_f32_16x16x128_f8f6f4 v[98:101], v[26:33], v[218:225], v[98:101]
	s_setprio 0
	s_barrier
	ds_read_b128 v[194:197], v180 offset:49152
	ds_read_b128 v[202:205], v180 offset:51200
	ds_read_b128 v[198:201], v181 offset:49152
	ds_read_b128 v[206:209], v181 offset:51200
	ds_read_b128 v[210:213], v180 offset:53248
	ds_read_b128 v[218:221], v180 offset:55296
	ds_read_b128 v[214:217], v181 offset:53248
	ds_read_b128 v[222:225], v181 offset:55296
	s_add_u32 s46, s66, 0x180
	s_addc_u32 s47, s67, 0
	s_mov_b32 m0, s52
	s_nop 0
	global_load_lds_dwordx4 v172, s[46:47] offset:0
	s_nop 0
	s_mov_b32 m0, s53
	s_nop 0
	global_load_lds_dwordx4 v173, s[46:47] offset:0
	s_add_u32 s46, s66, 0x20180
	s_addc_u32 s47, s67, 0
	s_mov_b32 m0, s56
	s_nop 0
	global_load_lds_dwordx4 v172, s[46:47] offset:0
	s_nop 0
	s_mov_b32 m0, s57
	s_nop 0
	global_load_lds_dwordx4 v173, s[46:47] offset:0
	s_add_u32 s46, s64, 0x180
	s_addc_u32 s47, s65, 0
	s_mov_b32 m0, s54
	s_nop 0
	global_load_lds_dwordx4 v162, s[46:47] offset:0
	s_nop 0
	s_mov_b32 m0, s55
	s_nop 0
	global_load_lds_dwordx4 v170, s[46:47] offset:0
	s_waitcnt vmcnt(8)
	s_waitcnt lgkmcnt(0)
	s_barrier
	s_setprio 1
	s_waitcnt lgkmcnt(5)
	v_mfma_f32_16x16x128_f8f6f4 v[94:97], v[2:9], v[194:201], v[94:97]
	v_mfma_f32_16x16x128_f8f6f4 v[90:93], v[10:17], v[194:201], v[90:93]
	s_waitcnt lgkmcnt(4)
	v_mfma_f32_16x16x128_f8f6f4 v[78:81], v[2:9], v[202:209], v[78:81]
	v_mfma_f32_16x16x128_f8f6f4 v[74:77], v[10:17], v[202:209], v[74:77]
	s_waitcnt lgkmcnt(1)
	v_mfma_f32_16x16x128_f8f6f4 v[62:65], v[2:9], v[210:217], v[62:65]
	v_mfma_f32_16x16x128_f8f6f4 v[58:61], v[10:17], v[210:217], v[58:61]
	s_waitcnt lgkmcnt(0)
	v_mfma_f32_16x16x128_f8f6f4 v[46:49], v[2:9], v[218:225], v[46:49]
	v_mfma_f32_16x16x128_f8f6f4 v[42:45], v[10:17], v[218:225], v[42:45]
	s_setprio 0
	s_setprio 1
	v_mfma_f32_16x16x128_f8f6f4 v[86:89], v[18:25], v[194:201], v[86:89]
	v_mfma_f32_16x16x128_f8f6f4 v[82:85], v[26:33], v[194:201], v[82:85]
	v_mfma_f32_16x16x128_f8f6f4 v[70:73], v[18:25], v[202:209], v[70:73]
	v_mfma_f32_16x16x128_f8f6f4 v[66:69], v[26:33], v[202:209], v[66:69]
	v_mfma_f32_16x16x128_f8f6f4 v[54:57], v[18:25], v[210:217], v[54:57]
	v_mfma_f32_16x16x128_f8f6f4 v[50:53], v[26:33], v[210:217], v[50:53]
	v_mfma_f32_16x16x128_f8f6f4 v[38:41], v[18:25], v[218:225], v[38:41]
	v_mfma_f32_16x16x128_f8f6f4 v[34:37], v[26:33], v[218:225], v[34:37]
	s_setprio 0
	s_add_i32 s35, s35, 2
	s_add_u32 s4, s4, 0x100
	s_addc_u32 s5, s5, 0
	s_barrier
.LBB0_650:
	.p2align 5
	s_nop 0
	ds_read_b128 v[18:21], v176
	ds_read_b128 v[26:29], v176 offset:2048
	ds_read_b128 v[22:25], v177
	ds_read_b128 v[30:33], v177 offset:2048
	ds_read_b128 v[2:5], v178
	ds_read_b128 v[10:13], v178 offset:2048
	ds_read_b128 v[6:9], v179
	ds_read_b128 v[14:17], v179 offset:2048
	ds_read_b128 v[194:197], v180
	ds_read_b128 v[202:205], v180 offset:2048
	ds_read_b128 v[198:201], v181
	ds_read_b128 v[206:209], v181 offset:2048
	ds_read_b128 v[210:213], v180 offset:4096
	ds_read_b128 v[218:221], v180 offset:6144
	ds_read_b128 v[214:217], v181 offset:4096
	ds_read_b128 v[222:225], v181 offset:6144
	s_add_u32 s64, s12, s4
	s_addc_u32 s65, s13, s5
	s_add_u32 s46, s64, 0x80
	s_addc_u32 s47, s65, 0
	s_mov_b32 m0, s58
	s_nop 0
	global_load_lds_dwordx4 v163, s[46:47] offset:0
	s_nop 0
	s_mov_b32 m0, s59
	s_nop 0
	global_load_lds_dwordx4 v171, s[46:47] offset:0
	s_waitcnt vmcnt(8)
	s_waitcnt lgkmcnt(0)
	s_barrier
	s_setprio 1
	s_waitcnt lgkmcnt(0)
	v_mfma_f32_16x16x128_f8f6f4 v[158:161], v[18:25], v[194:201], v[158:161]
	v_mfma_f32_16x16x128_f8f6f4 v[154:157], v[26:33], v[194:201], v[154:157]
	v_mfma_f32_16x16x128_f8f6f4 v[142:145], v[18:25], v[202:209], v[142:145]
	v_mfma_f32_16x16x128_f8f6f4 v[138:141], v[26:33], v[202:209], v[138:141]
	v_mfma_f32_16x16x128_f8f6f4 v[126:129], v[18:25], v[210:217], v[126:129]
	v_mfma_f32_16x16x128_f8f6f4 v[122:125], v[26:33], v[210:217], v[122:125]
	v_mfma_f32_16x16x128_f8f6f4 v[110:113], v[18:25], v[218:225], v[110:113]
	v_mfma_f32_16x16x128_f8f6f4 v[106:109], v[26:33], v[218:225], v[106:109]
	s_setprio 0
	s_setprio 1
	v_mfma_f32_16x16x128_f8f6f4 v[150:153], v[2:9], v[194:201], v[150:153]
	v_mfma_f32_16x16x128_f8f6f4 v[146:149], v[10:17], v[194:201], v[146:149]
	v_mfma_f32_16x16x128_f8f6f4 v[134:137], v[2:9], v[202:209], v[134:137]
	v_mfma_f32_16x16x128_f8f6f4 v[130:133], v[10:17], v[202:209], v[130:133]
	v_mfma_f32_16x16x128_f8f6f4 v[118:121], v[2:9], v[210:217], v[118:121]
	v_mfma_f32_16x16x128_f8f6f4 v[114:117], v[10:17], v[210:217], v[114:117]
	v_mfma_f32_16x16x128_f8f6f4 v[102:105], v[2:9], v[218:225], v[102:105]
	v_mfma_f32_16x16x128_f8f6f4 v[98:101], v[10:17], v[218:225], v[98:101]
	s_setprio 0
	s_barrier
	s_add_u32 s66, s42, s4
	s_addc_u32 s67, s43, s5
	ds_read_b128 v[194:197], v180 offset:16384
	ds_read_b128 v[202:205], v180 offset:18432
	ds_read_b128 v[198:201], v181 offset:16384
	ds_read_b128 v[206:209], v181 offset:18432
	ds_read_b128 v[210:213], v180 offset:20480
	ds_read_b128 v[218:221], v180 offset:22528
	ds_read_b128 v[214:217], v181 offset:20480
	ds_read_b128 v[222:225], v181 offset:22528
	s_add_u32 s46, s66, 0x100
	s_addc_u32 s47, s67, 0
	s_mov_b32 m0, s33
	s_nop 0
	global_load_lds_dwordx4 v172, s[46:47] offset:0
	s_nop 0
	s_mov_b32 m0, s39
	s_nop 0
	global_load_lds_dwordx4 v173, s[46:47] offset:0
	s_add_u32 s46, s66, 0x20100
	s_addc_u32 s47, s67, 0
	s_mov_b32 m0, s41
	s_nop 0
	global_load_lds_dwordx4 v172, s[46:47] offset:0
	s_nop 0
	s_mov_b32 m0, s48
	s_nop 0
	global_load_lds_dwordx4 v173, s[46:47] offset:0
	s_add_u32 s46, s64, 0x100
	s_addc_u32 s47, s65, 0
	s_mov_b32 m0, s1
	s_nop 0
	global_load_lds_dwordx4 v162, s[46:47] offset:0
	s_nop 0
	s_mov_b32 m0, s49
	s_nop 0
	global_load_lds_dwordx4 v170, s[46:47] offset:0
	s_waitcnt vmcnt(8)
	s_waitcnt lgkmcnt(0)
	s_barrier
	s_setprio 1
	s_waitcnt lgkmcnt(5)
	v_mfma_f32_16x16x128_f8f6f4 v[94:97], v[18:25], v[194:201], v[94:97]
	v_mfma_f32_16x16x128_f8f6f4 v[90:93], v[26:33], v[194:201], v[90:93]
	s_waitcnt lgkmcnt(4)
	v_mfma_f32_16x16x128_f8f6f4 v[78:81], v[18:25], v[202:209], v[78:81]
	v_mfma_f32_16x16x128_f8f6f4 v[74:77], v[26:33], v[202:209], v[74:77]
	s_waitcnt lgkmcnt(1)
	v_mfma_f32_16x16x128_f8f6f4 v[62:65], v[18:25], v[210:217], v[62:65]
	v_mfma_f32_16x16x128_f8f6f4 v[58:61], v[26:33], v[210:217], v[58:61]
	s_waitcnt lgkmcnt(0)
	v_mfma_f32_16x16x128_f8f6f4 v[46:49], v[18:25], v[218:225], v[46:49]
	v_mfma_f32_16x16x128_f8f6f4 v[42:45], v[26:33], v[218:225], v[42:45]
	s_setprio 0
	s_setprio 1
	v_mfma_f32_16x16x128_f8f6f4 v[86:89], v[2:9], v[194:201], v[86:89]
	v_mfma_f32_16x16x128_f8f6f4 v[82:85], v[10:17], v[194:201], v[82:85]
	v_mfma_f32_16x16x128_f8f6f4 v[70:73], v[2:9], v[202:209], v[70:73]
	v_mfma_f32_16x16x128_f8f6f4 v[66:69], v[10:17], v[202:209], v[66:69]
	v_mfma_f32_16x16x128_f8f6f4 v[54:57], v[2:9], v[210:217], v[54:57]
	v_mfma_f32_16x16x128_f8f6f4 v[50:53], v[10:17], v[210:217], v[50:53]
	v_mfma_f32_16x16x128_f8f6f4 v[38:41], v[2:9], v[218:225], v[38:41]
	v_mfma_f32_16x16x128_f8f6f4 v[34:37], v[10:17], v[218:225], v[34:37]
	s_setprio 0
	s_barrier
	s_add_i32 s68, 0, 0x18000
	v_add_u32_e32 v183, s68, v174
	v_add_u32_e32 v184, s68, v175
	s_add_i32 s68, 0, 0x1c000
	v_add_u32_e32 v185, s68, v174
	ds_read_b128 v[2:5], v183
	ds_read_b128 v[10:13], v183 offset:2048
	ds_read_b128 v[6:9], v184
	ds_read_b128 v[14:17], v184 offset:2048
	v_add_u32_e32 v186, s68, v175
	ds_read_b128 v[18:21], v185
	ds_read_b128 v[26:29], v185 offset:2048
	ds_read_b128 v[22:25], v186
	ds_read_b128 v[30:33], v186 offset:2048
	ds_read_b128 v[194:197], v180 offset:32768
	ds_read_b128 v[202:205], v180 offset:34816
	ds_read_b128 v[198:201], v181 offset:32768
	ds_read_b128 v[206:209], v181 offset:34816
	ds_read_b128 v[210:213], v180 offset:36864
	ds_read_b128 v[218:221], v180 offset:38912
	ds_read_b128 v[214:217], v181 offset:36864
	ds_read_b128 v[222:225], v181 offset:38912
	s_mov_b32 m0, s50
	s_nop 0
	global_load_lds_dwordx4 v163, s[46:47] offset:0
	s_nop 0
	s_mov_b32 m0, s51
	s_nop 0
	global_load_lds_dwordx4 v171, s[46:47] offset:0
	s_waitcnt vmcnt(8)
	s_waitcnt lgkmcnt(0)
	s_barrier
	s_setprio 1
	s_waitcnt lgkmcnt(5)
	v_mfma_f32_16x16x128_f8f6f4 v[158:161], v[2:9], v[194:201], v[158:161]
	v_mfma_f32_16x16x128_f8f6f4 v[154:157], v[10:17], v[194:201], v[154:157]
	s_waitcnt lgkmcnt(4)
	v_mfma_f32_16x16x128_f8f6f4 v[142:145], v[2:9], v[202:209], v[142:145]
	v_mfma_f32_16x16x128_f8f6f4 v[138:141], v[10:17], v[202:209], v[138:141]
	s_waitcnt lgkmcnt(1)
	v_mfma_f32_16x16x128_f8f6f4 v[126:129], v[2:9], v[210:217], v[126:129]
	v_mfma_f32_16x16x128_f8f6f4 v[122:125], v[10:17], v[210:217], v[122:125]
	s_waitcnt lgkmcnt(0)
	v_mfma_f32_16x16x128_f8f6f4 v[110:113], v[2:9], v[218:225], v[110:113]
	v_mfma_f32_16x16x128_f8f6f4 v[106:109], v[10:17], v[218:225], v[106:109]
	s_setprio 0
	s_setprio 1
	v_mfma_f32_16x16x128_f8f6f4 v[150:153], v[18:25], v[194:201], v[150:153]
	v_mfma_f32_16x16x128_f8f6f4 v[146:149], v[26:33], v[194:201], v[146:149]
	v_mfma_f32_16x16x128_f8f6f4 v[134:137], v[18:25], v[202:209], v[134:137]
	v_mfma_f32_16x16x128_f8f6f4 v[130:133], v[26:33], v[202:209], v[130:133]
	v_mfma_f32_16x16x128_f8f6f4 v[118:121], v[18:25], v[210:217], v[118:121]
	v_mfma_f32_16x16x128_f8f6f4 v[114:117], v[26:33], v[210:217], v[114:117]
	v_mfma_f32_16x16x128_f8f6f4 v[102:105], v[18:25], v[218:225], v[102:105]
	v_mfma_f32_16x16x128_f8f6f4 v[98:101], v[26:33], v[218:225], v[98:101]
	s_setprio 0
	s_barrier
	ds_read_b128 v[194:197], v180 offset:49152
	ds_read_b128 v[202:205], v180 offset:51200
	ds_read_b128 v[198:201], v181 offset:49152
	ds_read_b128 v[206:209], v181 offset:51200
	ds_read_b128 v[210:213], v180 offset:53248
	ds_read_b128 v[218:221], v180 offset:55296
	ds_read_b128 v[214:217], v181 offset:53248
	ds_read_b128 v[222:225], v181 offset:55296
	s_add_u32 s46, s66, 0x180
	s_addc_u32 s47, s67, 0
	s_mov_b32 m0, s52
	s_nop 0
	global_load_lds_dwordx4 v172, s[46:47] offset:0
	s_nop 0
	s_mov_b32 m0, s53
	s_nop 0
	global_load_lds_dwordx4 v173, s[46:47] offset:0
	s_add_u32 s46, s66, 0x20180
	s_addc_u32 s47, s67, 0
	s_mov_b32 m0, s56
	s_nop 0
	global_load_lds_dwordx4 v172, s[46:47] offset:0
	s_nop 0
	s_mov_b32 m0, s57
	s_nop 0
	global_load_lds_dwordx4 v173, s[46:47] offset:0
	s_add_u32 s46, s64, 0x180
	s_addc_u32 s47, s65, 0
	s_mov_b32 m0, s54
	s_nop 0
	global_load_lds_dwordx4 v162, s[46:47] offset:0
	s_nop 0
	s_mov_b32 m0, s55
	s_nop 0
	global_load_lds_dwordx4 v170, s[46:47] offset:0
	s_waitcnt vmcnt(8)
	s_waitcnt lgkmcnt(0)
	s_barrier
	s_setprio 1
	s_waitcnt lgkmcnt(5)
	v_mfma_f32_16x16x128_f8f6f4 v[94:97], v[2:9], v[194:201], v[94:97]
	v_mfma_f32_16x16x128_f8f6f4 v[90:93], v[10:17], v[194:201], v[90:93]
	s_waitcnt lgkmcnt(4)
	v_mfma_f32_16x16x128_f8f6f4 v[78:81], v[2:9], v[202:209], v[78:81]
	v_mfma_f32_16x16x128_f8f6f4 v[74:77], v[10:17], v[202:209], v[74:77]
	s_waitcnt lgkmcnt(1)
	v_mfma_f32_16x16x128_f8f6f4 v[62:65], v[2:9], v[210:217], v[62:65]
	v_mfma_f32_16x16x128_f8f6f4 v[58:61], v[10:17], v[210:217], v[58:61]
	s_waitcnt lgkmcnt(0)
	v_mfma_f32_16x16x128_f8f6f4 v[46:49], v[2:9], v[218:225], v[46:49]
	v_mfma_f32_16x16x128_f8f6f4 v[42:45], v[10:17], v[218:225], v[42:45]
	s_setprio 0
	s_setprio 1
	v_mfma_f32_16x16x128_f8f6f4 v[86:89], v[18:25], v[194:201], v[86:89]
	v_mfma_f32_16x16x128_f8f6f4 v[82:85], v[26:33], v[194:201], v[82:85]
	v_mfma_f32_16x16x128_f8f6f4 v[70:73], v[18:25], v[202:209], v[70:73]
	v_mfma_f32_16x16x128_f8f6f4 v[66:69], v[26:33], v[202:209], v[66:69]
	v_mfma_f32_16x16x128_f8f6f4 v[54:57], v[18:25], v[210:217], v[54:57]
	v_mfma_f32_16x16x128_f8f6f4 v[50:53], v[26:33], v[210:217], v[50:53]
	v_mfma_f32_16x16x128_f8f6f4 v[38:41], v[18:25], v[218:225], v[38:41]
	v_mfma_f32_16x16x128_f8f6f4 v[34:37], v[26:33], v[218:225], v[34:37]
	s_setprio 0
	s_add_i32 s35, s35, 2
	s_add_u32 s4, s4, 0x100
	s_addc_u32 s5, s5, 0
	s_cmp_lt_u32 s35, 4
	s_barrier
	s_cbranch_scc1 .LBB0_650
	ds_read_b128 v[18:21], v176
	ds_read_b128 v[26:29], v176 offset:2048
	ds_read_b128 v[22:25], v177
	ds_read_b128 v[30:33], v177 offset:2048
	ds_read_b128 v[2:5], v178
	ds_read_b128 v[10:13], v178 offset:2048
	ds_read_b128 v[6:9], v179
	ds_read_b128 v[14:17], v179 offset:2048
	ds_read_b128 v[194:197], v180
	ds_read_b128 v[202:205], v180 offset:2048
	ds_read_b128 v[198:201], v181
	ds_read_b128 v[206:209], v181 offset:2048
	ds_read_b128 v[210:213], v180 offset:4096
	ds_read_b128 v[218:221], v180 offset:6144
	ds_read_b128 v[214:217], v181 offset:4096
	ds_read_b128 v[222:225], v181 offset:6144
	s_mov_b32 m0, s58
	s_nop 0
	global_load_lds_dwordx4 v163, s[24:25] offset:0
	s_nop 0
	s_mov_b32 m0, s59
	s_nop 0
	global_load_lds_dwordx4 v171, s[24:25] offset:0
	s_waitcnt vmcnt(8)
	s_waitcnt lgkmcnt(0)
	s_barrier
	s_setprio 1
	s_waitcnt lgkmcnt(5)
	v_mfma_f32_16x16x128_f8f6f4 v[158:161], v[18:25], v[194:201], v[158:161]
	v_mfma_f32_16x16x128_f8f6f4 v[154:157], v[26:33], v[194:201], v[154:157]
	s_waitcnt lgkmcnt(4)
	v_mfma_f32_16x16x128_f8f6f4 v[142:145], v[18:25], v[202:209], v[142:145]
	v_mfma_f32_16x16x128_f8f6f4 v[138:141], v[26:33], v[202:209], v[138:141]
	s_waitcnt lgkmcnt(1)
	v_mfma_f32_16x16x128_f8f6f4 v[126:129], v[18:25], v[210:217], v[126:129]
	v_mfma_f32_16x16x128_f8f6f4 v[122:125], v[26:33], v[210:217], v[122:125]
	s_waitcnt lgkmcnt(0)
	v_mfma_f32_16x16x128_f8f6f4 v[110:113], v[18:25], v[218:225], v[110:113]
	v_mfma_f32_16x16x128_f8f6f4 v[106:109], v[26:33], v[218:225], v[106:109]
	s_setprio 0
	s_setprio 1
	v_mfma_f32_16x16x128_f8f6f4 v[150:153], v[2:9], v[194:201], v[150:153]
	v_mfma_f32_16x16x128_f8f6f4 v[146:149], v[10:17], v[194:201], v[146:149]
	v_mfma_f32_16x16x128_f8f6f4 v[134:137], v[2:9], v[202:209], v[134:137]
	v_mfma_f32_16x16x128_f8f6f4 v[130:133], v[10:17], v[202:209], v[130:133]
	v_mfma_f32_16x16x128_f8f6f4 v[118:121], v[2:9], v[210:217], v[118:121]
	v_mfma_f32_16x16x128_f8f6f4 v[114:117], v[10:17], v[210:217], v[114:117]
	v_mfma_f32_16x16x128_f8f6f4 v[102:105], v[2:9], v[218:225], v[102:105]
	v_mfma_f32_16x16x128_f8f6f4 v[98:101], v[10:17], v[218:225], v[98:101]
	s_setprio 0
	s_barrier
	v_cndmask_b32_e64 v187, 0, 1, s[44:45]
	v_cmp_ne_u32_e64 s[4:5], 1, v187
	s_andn2_b64 vcc, exec, s[44:45]
	s_cbranch_vccnz .LBB0_653
	v_mov_b32_e32 v162, v0
	s_nop 0
	v_lshlrev_b32_e32 v163, 4, v162
	v_bitop3_b32 v163, v163, s0, v162 bitop3:0x48
	v_lshlrev_b32_e32 v162, 7, v162
	v_lshl_or_b32 v163, s61, 18, v163
	v_and_b32_e32 v162, 0xfffffc00, v162
	v_add_u32_e32 v162, v163, v162
	v_add_u32_e32 v163, 0x20000, v162
	v_add_u32_e32 v170, 0x10000, v162
	v_add_u32_e32 v171, 0x30000, v162
